# stack: lane-linear Y/z + attention QK fragment prefetch + K-tile-major int8 weights (contiguous B-side DMA) + gate-epilogue VALU trims (log2e fold, pk_add)
# speedup vs baseline: 1.0044x; 1.0044x over previous
; __device__ __forceinline__ unsigned pk2h(float lo, float hi) { f32x2 v = {lo, hi}; f16x2 h = __builtin_convertvector(v, f16x2); return __builtin_bit_cast(unsigned, h); }
; #define PG8_LAS __attribute__((address_space(3)))
;     __device__ __forceinline__ void operator()(const f32x4 (&acc)[2][2][4][2], const Unit& u, int wr, int wc, int fr, int fq) const {
;     ...
;         const int b = (u.pm * BM) / SEQ; float rs[2][4]; row_rstd(u, wr, fr, rs);
;         f32x4 bv[2][2];
; #pragma unroll
;         for (int bj = 0; bj < 2; ++bj)
; #pragma unroll
;             for (int n = 0; n < 2; ++n) bv[bj][n] = *(const PG8_LAS f32x4*)(uintptr_t)(CV_LDS + u.idx * 1024 + (wc * 32 + 8 * fq + bj * HALF + 4 * n) * 4);
;     ...
;                 for (int bj = 0; bj < 2; ++bj) {
;                     f32x4 a0 = acc[ai][bj][m][0], a1 = acc[ai][bj][m][1];
;                     if constexpr (I8) { const i32x4 i0 = __builtin_bit_cast(i32x4, a0), i1 = __builtin_bit_cast(i32x4, a1);
;                         a0 = (f32x4){(float)i0.x, (float)i0.y, (float)i0.z, (float)i0.w} * sv[bj][0]; a1 = (f32x4){(float)i1.x, (float)i1.y, (float)i1.z, (float)i1.w} * sv[bj][1]; }
;                     const f32x4 g0 = a0 * rs[ai][m] + bv[bj][0], g1 = a1 * rs[ai][m] + bv[bj][1];
;                     const f16x8 yy = yv[m][bj];
;                     float z[8];
; #pragma unroll
;                     for (int e = 0; e < 4; ++e) { z[e] = (float)yy[e] * __builtin_amdgcn_rcpf(1.f + __builtin_amdgcn_exp2f(-LOG2E * g0[e])); z[4 + e] = (float)yy[4 + e] * __builtin_amdgcn_rcpf(1.f + __builtin_amdgcn_exp2f(-LOG2E * g1[e])); }
;                     if (br == 2) {
; #pragma unroll
;                         for (int e = 0; e < 8; ++e) z[e] += (float)za[bj][e] + (float)zb[bj][e]; }
;                     u32x4 w; w.x = pk2h(z[0], z[1]); w.y = pk2h(z[2], z[3]); w.z = pk2h(z[4], z[5]); w.w = pk2h(z[6], z[7]);
;                     f16* dst = (br == 2) ? merged : Yb;
;                     gst16(dst + off + bj * HALF, w); } } } }
.LBB0_1231:
	s_waitcnt lgkmcnt(0)
	v_mul_f32_e32 v226, 0xbfb8aa3b, v226
	v_mul_f32_e32 v227, 0xbfb8aa3b, v227
	v_mul_f32_e32 v220, 0xbfb8aa3b, v220
	v_mul_f32_e32 v221, 0xbfb8aa3b, v221
	v_mul_f32_e32 v214, 0xbfb8aa3b, v214
	v_mul_f32_e32 v215, 0xbfb8aa3b, v215
	v_mul_f32_e32 v212, 0xbfb8aa3b, v212
	v_mul_f32_e32 v213, 0xbfb8aa3b, v213
	v_mul_f32_e32 v62, 0xbfb8aa3b, v62
	v_mul_f32_e32 v63, 0xbfb8aa3b, v63
	v_mul_f32_e32 v64, 0xbfb8aa3b, v64
	v_mul_f32_e32 v65, 0xbfb8aa3b, v65
	v_mul_f32_e32 v50, 0xbfb8aa3b, v50
	v_mul_f32_e32 v51, 0xbfb8aa3b, v51
	v_mul_f32_e32 v52, 0xbfb8aa3b, v52
	v_mul_f32_e32 v53, 0xbfb8aa3b, v53
	v_mul_f32_e32 v34, 0xbfb8aa3b, v34
	v_mul_f32_e32 v35, 0xbfb8aa3b, v35
	v_mul_f32_e32 v36, 0xbfb8aa3b, v36
	v_mul_f32_e32 v37, 0xbfb8aa3b, v37
	v_mul_f32_e32 v26, 0xbfb8aa3b, v26
	v_mul_f32_e32 v27, 0xbfb8aa3b, v27
	v_mul_f32_e32 v28, 0xbfb8aa3b, v28
	v_mul_f32_e32 v29, 0xbfb8aa3b, v29
	v_cvt_f32_i32_e32 v219, v178
	v_cvt_f32_i32_e32 v230, v179
	v_cvt_f32_i32_e32 v182, v182
	v_cvt_f32_i32_e32 v183, v183
	s_waitcnt lgkmcnt(2)
	v_mul_f32_e32 v179, v54, v219
	v_fma_f32 v179, v226, v179, v50
	v_exp_f32_e32 v179, v179
	v_cvt_f32_i32_e32 v231, v180
	v_mul_f32_e32 v178, v70, v182
	v_fma_f32 v178, v226, v178, v62
	v_add_f32_e32 v179, 1.0, v179
	v_rcp_f32_e32 v180, v179
	v_mul_f32_e32 v179, v71, v183
	v_fma_f32 v179, v226, v179, v63
	v_exp_f32_e32 v178, v178
	v_exp_f32_e32 v179, v179
	v_cvt_f32_i32_e32 v239, v181
	v_mul_f32_e32 v181, v55, v230
	v_fma_f32 v181, v226, v181, v51
	v_pk_add_f32 v[178:179], v[178:179], 1.0 op_sel_hi:[1,0]
	v_exp_f32_e32 v181, v181
	v_rcp_f32_e32 v178, v178
	v_rcp_f32_e32 v179, v179
	s_waitcnt vmcnt(3)
	v_cvt_f32_f16_sdwa v183, v190 dst_sel:DWORD dst_unused:UNUSED_PAD src0_sel:WORD_1
	v_cvt_f32_f16_e32 v182, v190
	v_add_f32_e32 v181, 1.0, v181
	v_rcp_f32_e32 v181, v181
	v_cvt_f32_i32_e32 v184, v184
	v_pk_mul_f32 v[178:179], v[178:179], v[182:183]
	v_cvt_f32_f16_sdwa v183, v192 dst_sel:DWORD dst_unused:UNUSED_PAD src0_sel:WORD_1
	v_cvt_f32_f16_e32 v182, v192
	v_cvt_f32_i32_e32 v185, v185
	v_cvt_f32_f16_sdwa v241, v191 dst_sel:DWORD dst_unused:UNUSED_PAD src0_sel:WORD_1
	v_cvt_f32_f16_e32 v240, v191
	v_pk_mul_f32 v[180:181], v[180:181], v[182:183]
	v_mul_f32_e32 v183, v56, v231
	v_fma_f32 v183, v226, v183, v52
	v_exp_f32_e32 v183, v183
	v_mul_f32_e32 v182, v72, v184
	v_fma_f32 v182, v226, v182, v64
	v_add_f32_e32 v183, 1.0, v183
	v_rcp_f32_e32 v184, v183
	v_mul_f32_e32 v183, v73, v185
	v_mul_f32_e32 v185, v57, v239
	v_fma_f32 v183, v226, v183, v65
	v_fma_f32 v185, v226, v185, v53
	v_exp_f32_e32 v182, v182
	v_exp_f32_e32 v183, v183
	v_exp_f32_e32 v185, v185
	v_cvt_f32_f16_sdwa v191, v193 dst_sel:DWORD dst_unused:UNUSED_PAD src0_sel:WORD_1
	v_pk_add_f32 v[182:183], v[182:183], 1.0 op_sel_hi:[1,0]
	v_add_f32_e32 v185, 1.0, v185
	v_rcp_f32_e32 v182, v182
	v_rcp_f32_e32 v183, v183
	v_rcp_f32_e32 v185, v185
	v_cvt_f32_f16_e32 v190, v193
	v_readlane_b32 s90, v255, 17
	v_readlane_b32 s91, v255, 18
	v_pk_mul_f32 v[182:183], v[182:183], v[240:241]
	v_pk_mul_f32 v[184:185], v[184:185], v[190:191]
	s_and_b64 vcc, exec, s[36:37]
	s_cbranch_vccnz .LBB0_1233
	v_cvt_f32_f16_sdwa v191, v58 dst_sel:DWORD dst_unused:UNUSED_PAD src0_sel:WORD_1
	v_cvt_f32_f16_e32 v190, v58
	s_waitcnt vmcnt(1)
	v_cvt_f32_f16_sdwa v193, v66 dst_sel:DWORD dst_unused:UNUSED_PAD src0_sel:WORD_1
	v_cvt_f32_f16_e32 v192, v66
	v_cvt_f32_f16_sdwa v241, v59 dst_sel:DWORD dst_unused:UNUSED_PAD src0_sel:WORD_1
	v_cvt_f32_f16_e32 v240, v59
	v_cvt_f32_f16_sdwa v247, v67 dst_sel:DWORD dst_unused:UNUSED_PAD src0_sel:WORD_1
	v_cvt_f32_f16_e32 v246, v67
	v_cvt_f32_f16_sdwa v249, v60 dst_sel:DWORD dst_unused:UNUSED_PAD src0_sel:WORD_1
	v_cvt_f32_f16_e32 v248, v60
	v_mov_b32_e32 v239, v243
	v_cvt_f32_f16_sdwa v243, v68 dst_sel:DWORD dst_unused:UNUSED_PAD src0_sel:WORD_1
	v_mov_b32_e32 v219, v242
	v_cvt_f32_f16_e32 v242, v68
	v_mov_b64_e32 v[222:223], v[216:217]
	v_mov_b64_e32 v[216:217], v[200:201]
	v_mov_b64_e32 v[200:201], v[250:251]
	v_cvt_f32_f16_sdwa v251, v61 dst_sel:DWORD dst_unused:UNUSED_PAD src0_sel:WORD_1
	v_cvt_f32_f16_e32 v250, v61
	v_cvt_f32_f16_sdwa v231, v69 dst_sel:DWORD dst_unused:UNUSED_PAD src0_sel:WORD_1
	v_cvt_f32_f16_e32 v230, v69
	v_mov_b32_e32 v198, v245
	v_mov_b32_e32 v245, v236
	v_mov_b32_e32 v236, v208
	v_mov_b32_e32 v208, v197
	v_mov_b32_e32 v197, v235
	v_mov_b32_e32 v235, v237
	v_mov_b32_e32 v237, v205
	v_mov_b32_e32 v205, v206
	v_pk_add_f32 v[190:191], v[192:193], v[190:191]
	v_pk_add_f32 v[192:193], v[246:247], v[240:241]
	v_pk_add_f32 v[240:241], v[242:243], v[248:249]
	v_pk_add_f32 v[230:231], v[230:231], v[250:251]
	v_mov_b32_e32 v243, v239
	v_mov_b32_e32 v242, v219
	v_mov_b32_e32 v206, v205
	v_mov_b32_e32 v205, v237
	v_mov_b32_e32 v237, v235
	v_mov_b32_e32 v235, v197
	v_mov_b32_e32 v197, v208
	v_mov_b32_e32 v208, v236
	v_mov_b32_e32 v236, v245
	v_mov_b32_e32 v245, v198
	v_mov_b64_e32 v[250:251], v[200:201]
	v_mov_b64_e32 v[200:201], v[216:217]
	v_mov_b64_e32 v[216:217], v[222:223]
	v_pk_add_f32 v[178:179], v[178:179], v[190:191]
	v_pk_add_f32 v[182:183], v[182:183], v[192:193]
	v_pk_add_f32 v[180:181], v[180:181], v[240:241]
	v_pk_add_f32 v[184:185], v[184:185], v[230:231]
	s_mov_b64 s[46:47], s[42:43]
	s_branch .LBB0_1234

; __device__ __forceinline__ unsigned pk2h(float lo, float hi) { f32x2 v = {lo, hi}; f16x2 h = __builtin_convertvector(v, f16x2); return __builtin_bit_cast(unsigned, h); }
;     __device__ __forceinline__ void operator()(const f32x4 (&acc)[2][2][4][2], const Unit& u, int wr, int wc, int fr, int fq) const {
;     ...
;                 for (int bj = 0; bj < 2; ++bj) {
;                     f32x4 a0 = acc[ai][bj][m][0], a1 = acc[ai][bj][m][1];
;                     if constexpr (I8) { const i32x4 i0 = __builtin_bit_cast(i32x4, a0), i1 = __builtin_bit_cast(i32x4, a1);
;                         a0 = (f32x4){(float)i0.x, (float)i0.y, (float)i0.z, (float)i0.w} * sv[bj][0]; a1 = (f32x4){(float)i1.x, (float)i1.y, (float)i1.z, (float)i1.w} * sv[bj][1]; }
;                     const f32x4 g0 = a0 * rs[ai][m] + bv[bj][0], g1 = a1 * rs[ai][m] + bv[bj][1];
;                     const f16x8 yy = yv[m][bj];
;                     float z[8];
; #pragma unroll
;                     for (int e = 0; e < 4; ++e) { z[e] = (float)yy[e] * __builtin_amdgcn_rcpf(1.f + __builtin_amdgcn_exp2f(-LOG2E * g0[e])); z[4 + e] = (float)yy[4 + e] * __builtin_amdgcn_rcpf(1.f + __builtin_amdgcn_exp2f(-LOG2E * g1[e])); }
;                     if (br == 2) {
; #pragma unroll
;                         for (int e = 0; e < 8; ++e) z[e] += (float)za[bj][e] + (float)zb[bj][e]; }
;                     u32x4 w; w.x = pk2h(z[0], z[1]); w.y = pk2h(z[2], z[3]); w.z = pk2h(z[4], z[5]); w.w = pk2h(z[6], z[7]);
;                     f16* dst = (br == 2) ? merged : Yb;
;                     gst16(dst + off + bj * HALF, w); } } } }
.LBB0_1234:
	v_cvt_pk_f16_f32 v192, v180, v181
	v_cvt_f32_i32_e32 v180, v172
	v_cvt_f32_i32_e32 v172, v166
	v_cvt_pk_f16_f32 v191, v182, v183
	v_cvt_f32_i32_e32 v182, v167
	v_cvt_f32_i32_e32 v170, v170
	s_waitcnt lgkmcnt(0)
	v_mul_f32_e32 v167, v30, v172
	v_fma_f32 v167, v226, v167, v26
	v_exp_f32_e32 v167, v167
	v_cvt_f32_i32_e32 v171, v171
	v_mul_f32_e32 v166, v38, v170
	v_fma_f32 v166, v226, v166, v34
	v_add_f32_e32 v167, 1.0, v167
	v_rcp_f32_e32 v170, v167
	v_mul_f32_e32 v167, v39, v171
	v_fma_f32 v167, v226, v167, v35
	v_exp_f32_e32 v166, v166
	v_exp_f32_e32 v167, v167
	v_mul_f32_e32 v171, v31, v182
	v_fma_f32 v171, v226, v171, v27
	v_pk_add_f32 v[166:167], v[166:167], 1.0 op_sel_hi:[1,0]
	v_exp_f32_e32 v171, v171
	v_cvt_f32_i32_e32 v181, v173
	v_rcp_f32_e32 v166, v166
	v_rcp_f32_e32 v167, v167
	s_waitcnt vmcnt(2)
	v_cvt_f32_f16_sdwa v173, v186 dst_sel:DWORD dst_unused:UNUSED_PAD src0_sel:WORD_1
	v_cvt_f32_f16_e32 v172, v186
	v_add_f32_e32 v171, 1.0, v171
	v_rcp_f32_e32 v171, v171
	v_cvt_pk_f16_f32 v190, v178, v179
	v_pk_mul_f32 v[166:167], v[166:167], v[172:173]
	v_cvt_f32_f16_sdwa v173, v188 dst_sel:DWORD dst_unused:UNUSED_PAD src0_sel:WORD_1
	v_cvt_f32_f16_e32 v172, v188
	v_cvt_pk_f16_f32 v193, v184, v185
	v_lshl_add_u64 v[178:179], v[228:229], 1, s[46:47]
	s_mov_b64 s[52:53], -1
	v_pk_mul_f32 v[170:171], v[170:171], v[172:173]
	v_mul_f32_e32 v172, v40, v180
	v_mul_f32_e32 v173, v41, v181
	v_fma_f32 v172, v226, v172, v36
	v_fma_f32 v173, v226, v173, v37
	v_exp_f32_e32 v172, v172
	v_exp_f32_e32 v173, v173
	v_cvt_f32_f16_sdwa v181, v187 dst_sel:DWORD dst_unused:UNUSED_PAD src0_sel:WORD_1
	v_cvt_f32_f16_e32 v180, v187
	v_pk_add_f32 v[172:173], v[172:173], 1.0 op_sel_hi:[1,0]
	v_rcp_f32_e32 v172, v172
	v_rcp_f32_e32 v173, v173
	s_andn2_b64 vcc, exec, s[50:51]
	v_mov_b32_e32 v222, v224
	v_mov_b32_e32 v223, v225
	v_cndmask_b32_e64 v222, v178, v222, s[36:37]
	v_cndmask_b32_e64 v223, v179, v223, s[36:37]
	global_store_dwordx4 v[222:223], v[190:193], off
	v_pk_mul_f32 v[172:173], v[172:173], v[180:181]
	v_cndmask_b32_e64 v180, 0, 1, s[50:51]
	v_cmp_ne_u32_e64 s[38:39], 1, v180
	s_cbranch_vccnz .LBB0_1236
	s_mov_b64 s[52:53], 0
.LBB0_1236:
	v_cvt_f32_i32_e32 v168, v168
	v_cvt_f32_i32_e32 v169, v169
	v_cvt_f32_f16_sdwa v181, v189 dst_sel:DWORD dst_unused:UNUSED_PAD src0_sel:WORD_1
	v_cvt_f32_f16_e32 v180, v189
	v_mul_f32_e32 v168, v32, v168
	v_mul_f32_e32 v169, v33, v169
	v_fma_f32 v168, v226, v168, v28
	v_fma_f32 v169, v226, v169, v29
	v_exp_f32_e32 v168, v168
	v_exp_f32_e32 v169, v169
	s_andn2_b64 vcc, exec, s[52:53]
	v_pk_add_f32 v[168:169], v[168:169], 1.0 op_sel_hi:[1,0]
	v_rcp_f32_e32 v168, v168
	v_rcp_f32_e32 v169, v169
	s_nop 0
	v_pk_mul_f32 v[168:169], v[168:169], v[180:181]
	s_cbranch_vccnz .LBB0_1238
	v_cvt_f32_f16_sdwa v181, v42 dst_sel:DWORD dst_unused:UNUSED_PAD src0_sel:WORD_1
	v_cvt_f32_f16_e32 v180, v42
	s_waitcnt vmcnt(1)
	v_cvt_f32_f16_sdwa v183, v46 dst_sel:DWORD dst_unused:UNUSED_PAD src0_sel:WORD_1
	v_cvt_f32_f16_e32 v182, v46
	v_cvt_f32_f16_sdwa v185, v43 dst_sel:DWORD dst_unused:UNUSED_PAD src0_sel:WORD_1
	v_cvt_f32_f16_e32 v184, v43
	v_cvt_f32_f16_sdwa v187, v47 dst_sel:DWORD dst_unused:UNUSED_PAD src0_sel:WORD_1
	v_cvt_f32_f16_e32 v186, v47
	v_cvt_f32_f16_sdwa v189, v44 dst_sel:DWORD dst_unused:UNUSED_PAD src0_sel:WORD_1
	v_cvt_f32_f16_e32 v188, v44
	v_cvt_f32_f16_sdwa v191, v48 dst_sel:DWORD dst_unused:UNUSED_PAD src0_sel:WORD_1
	v_cvt_f32_f16_e32 v190, v48
	v_cvt_f32_f16_sdwa v193, v45 dst_sel:DWORD dst_unused:UNUSED_PAD src0_sel:WORD_1
	v_cvt_f32_f16_e32 v192, v45
	v_cvt_f32_f16_sdwa v231, v49 dst_sel:DWORD dst_unused:UNUSED_PAD src0_sel:WORD_1
	v_cvt_f32_f16_e32 v230, v49
	v_pk_add_f32 v[180:181], v[182:183], v[180:181]
	v_pk_add_f32 v[182:183], v[186:187], v[184:185]
	v_pk_add_f32 v[184:185], v[190:191], v[188:189]
	v_pk_add_f32 v[186:187], v[230:231], v[192:193]
	v_pk_add_f32 v[166:167], v[166:167], v[180:181]
	v_pk_add_f32 v[172:173], v[172:173], v[182:183]
	v_pk_add_f32 v[170:171], v[170:171], v[184:185]
	v_pk_add_f32 v[168:169], v[168:169], v[186:187]
	v_bfrev_b32_e32 v230, 1
	s_branch .LBB0_1239

; __device__ __forceinline__ unsigned pk2h(float lo, float hi) { f32x2 v = {lo, hi}; f16x2 h = __builtin_convertvector(v, f16x2); return __builtin_bit_cast(unsigned, h); }
;     __device__ __forceinline__ void operator()(const f32x4 (&acc)[2][2][4][2], const Unit& u, int wr, int wc, int fr, int fq) const {
;     ...
;                 for (int bj = 0; bj < 2; ++bj) {
;                     f32x4 a0 = acc[ai][bj][m][0], a1 = acc[ai][bj][m][1];
;                     if constexpr (I8) { const i32x4 i0 = __builtin_bit_cast(i32x4, a0), i1 = __builtin_bit_cast(i32x4, a1);
;                         a0 = (f32x4){(float)i0.x, (float)i0.y, (float)i0.z, (float)i0.w} * sv[bj][0]; a1 = (f32x4){(float)i1.x, (float)i1.y, (float)i1.z, (float)i1.w} * sv[bj][1]; }
;                     const f32x4 g0 = a0 * rs[ai][m] + bv[bj][0], g1 = a1 * rs[ai][m] + bv[bj][1];
;                     const f16x8 yy = yv[m][bj];
;                     float z[8];
; #pragma unroll
;                     for (int e = 0; e < 4; ++e) { z[e] = (float)yy[e] * __builtin_amdgcn_rcpf(1.f + __builtin_amdgcn_exp2f(-LOG2E * g0[e])); z[4 + e] = (float)yy[4 + e] * __builtin_amdgcn_rcpf(1.f + __builtin_amdgcn_exp2f(-LOG2E * g1[e])); }
;                     if (br == 2) {
; #pragma unroll
;                         for (int e = 0; e < 8; ++e) z[e] += (float)za[bj][e] + (float)zb[bj][e]; }
;                     u32x4 w; w.x = pk2h(z[0], z[1]); w.y = pk2h(z[2], z[3]); w.z = pk2h(z[4], z[5]); w.w = pk2h(z[6], z[7]);
;                     f16* dst = (br == 2) ? merged : Yb;
;                     gst16(dst + off + bj * HALF, w); } } } }
.LBB0_1241:
	v_cvt_f32_i32_e32 v166, v154
	v_cvt_f32_i32_e32 v167, v155
	v_cvt_f32_i32_e32 v158, v158
	v_cvt_f32_i32_e32 v159, v159
	v_mul_f32_e32 v155, v54, v166
	v_fma_f32 v155, v227, v155, v50
	v_exp_f32_e32 v155, v155
	v_cvt_f32_i32_e32 v168, v156
	v_mul_f32_e32 v154, v70, v158
	v_fma_f32 v154, v227, v154, v62
	v_add_f32_e32 v155, 1.0, v155
	v_rcp_f32_e32 v156, v155
	v_mul_f32_e32 v155, v71, v159
	v_fma_f32 v155, v227, v155, v63
	v_exp_f32_e32 v154, v154
	v_exp_f32_e32 v155, v155
	v_cvt_f32_i32_e32 v169, v157
	v_mul_f32_e32 v157, v55, v167
	v_fma_f32 v157, v227, v157, v51
	v_pk_add_f32 v[154:155], v[154:155], 1.0 op_sel_hi:[1,0]
	v_exp_f32_e32 v157, v157
	v_rcp_f32_e32 v154, v154
	v_rcp_f32_e32 v155, v155
	s_waitcnt vmcnt(3)
	v_cvt_f32_f16_sdwa v159, v174 dst_sel:DWORD dst_unused:UNUSED_PAD src0_sel:WORD_1
	v_cvt_f32_f16_e32 v158, v174
	v_add_f32_e32 v157, 1.0, v157
	v_rcp_f32_e32 v157, v157
	v_cvt_f32_i32_e32 v160, v160
	v_pk_mul_f32 v[154:155], v[154:155], v[158:159]
	v_cvt_f32_f16_sdwa v159, v176 dst_sel:DWORD dst_unused:UNUSED_PAD src0_sel:WORD_1
	v_cvt_f32_f16_e32 v158, v176
	v_cvt_f32_i32_e32 v161, v161
	v_cvt_f32_f16_sdwa v167, v175 dst_sel:DWORD dst_unused:UNUSED_PAD src0_sel:WORD_1
	v_cvt_f32_f16_e32 v166, v175
	v_pk_mul_f32 v[156:157], v[156:157], v[158:159]
	v_mul_f32_e32 v159, v56, v168
	v_fma_f32 v159, v227, v159, v52
	v_exp_f32_e32 v159, v159
	v_mul_f32_e32 v158, v72, v160
	v_fma_f32 v158, v227, v158, v64
	v_add_f32_e32 v159, 1.0, v159
	v_rcp_f32_e32 v160, v159
	v_mul_f32_e32 v159, v73, v161
	v_fma_f32 v159, v227, v159, v65
	v_exp_f32_e32 v158, v158
	v_exp_f32_e32 v159, v159
	v_mul_f32_e32 v161, v57, v169
	v_fma_f32 v161, v227, v161, v53
	v_pk_add_f32 v[158:159], v[158:159], 1.0 op_sel_hi:[1,0]
	v_exp_f32_e32 v161, v161
	v_rcp_f32_e32 v158, v158
	v_rcp_f32_e32 v159, v159
	s_and_b64 vcc, exec, s[36:37]
	v_add_f32_e32 v161, 1.0, v161
	v_rcp_f32_e32 v161, v161
	v_pk_mul_f32 v[158:159], v[158:159], v[166:167]
	v_cvt_f32_f16_sdwa v167, v177 dst_sel:DWORD dst_unused:UNUSED_PAD src0_sel:WORD_1
	v_cvt_f32_f16_e32 v166, v177
	v_pk_mul_f32 v[160:161], v[160:161], v[166:167]
	s_cbranch_vccnz .LBB0_1243
	v_cvt_f32_f16_sdwa v167, v58 dst_sel:DWORD dst_unused:UNUSED_PAD src0_sel:WORD_1
	v_cvt_f32_f16_e32 v166, v58
	s_waitcnt vmcnt(1)
	v_cvt_f32_f16_sdwa v169, v66 dst_sel:DWORD dst_unused:UNUSED_PAD src0_sel:WORD_1
	v_cvt_f32_f16_e32 v168, v66
	v_cvt_f32_f16_sdwa v171, v59 dst_sel:DWORD dst_unused:UNUSED_PAD src0_sel:WORD_1
	v_cvt_f32_f16_e32 v170, v59
	v_cvt_f32_f16_sdwa v173, v67 dst_sel:DWORD dst_unused:UNUSED_PAD src0_sel:WORD_1
	v_cvt_f32_f16_e32 v172, v67
	v_cvt_f32_f16_sdwa v175, v60 dst_sel:DWORD dst_unused:UNUSED_PAD src0_sel:WORD_1
	v_cvt_f32_f16_e32 v174, v60
	v_cvt_f32_f16_sdwa v177, v68 dst_sel:DWORD dst_unused:UNUSED_PAD src0_sel:WORD_1
	v_cvt_f32_f16_e32 v176, v68
	v_cvt_f32_f16_sdwa v181, v61 dst_sel:DWORD dst_unused:UNUSED_PAD src0_sel:WORD_1
	v_cvt_f32_f16_e32 v180, v61
	v_cvt_f32_f16_sdwa v183, v69 dst_sel:DWORD dst_unused:UNUSED_PAD src0_sel:WORD_1
	v_cvt_f32_f16_e32 v182, v69
	v_pk_add_f32 v[166:167], v[168:169], v[166:167]
	v_pk_add_f32 v[168:169], v[172:173], v[170:171]
	v_pk_add_f32 v[170:171], v[176:177], v[174:175]
	v_pk_add_f32 v[172:173], v[182:183], v[180:181]
	v_pk_add_f32 v[154:155], v[154:155], v[166:167]
	v_pk_add_f32 v[158:159], v[158:159], v[168:169]
	v_pk_add_f32 v[156:157], v[156:157], v[170:171]
	v_pk_add_f32 v[160:161], v[160:161], v[172:173]
; __device__ __forceinline__ unsigned pk2h(float lo, float hi) { f32x2 v = {lo, hi}; f16x2 h = __builtin_convertvector(v, f16x2); return __builtin_bit_cast(unsigned, h); }
;     __device__ __forceinline__ void operator()(const f32x4 (&acc)[2][2][4][2], const Unit& u, int wr, int wc, int fr, int fq) const {
;     ...
;                 for (int bj = 0; bj < 2; ++bj) {
;                     f32x4 a0 = acc[ai][bj][m][0], a1 = acc[ai][bj][m][1];
;                     if constexpr (I8) { const i32x4 i0 = __builtin_bit_cast(i32x4, a0), i1 = __builtin_bit_cast(i32x4, a1);
;                         a0 = (f32x4){(float)i0.x, (float)i0.y, (float)i0.z, (float)i0.w} * sv[bj][0]; a1 = (f32x4){(float)i1.x, (float)i1.y, (float)i1.z, (float)i1.w} * sv[bj][1]; }
;                     const f32x4 g0 = a0 * rs[ai][m] + bv[bj][0], g1 = a1 * rs[ai][m] + bv[bj][1];
;                     const f16x8 yy = yv[m][bj];
;                     float z[8];
; #pragma unroll
;                     for (int e = 0; e < 4; ++e) { z[e] = (float)yy[e] * __builtin_amdgcn_rcpf(1.f + __builtin_amdgcn_exp2f(-LOG2E * g0[e])); z[4 + e] = (float)yy[4 + e] * __builtin_amdgcn_rcpf(1.f + __builtin_amdgcn_exp2f(-LOG2E * g1[e])); }
;                     if (br == 2) {
; #pragma unroll
;                         for (int e = 0; e < 8; ++e) z[e] += (float)za[bj][e] + (float)zb[bj][e]; }
;                     u32x4 w; w.x = pk2h(z[0], z[1]); w.y = pk2h(z[2], z[3]); w.z = pk2h(z[4], z[5]); w.w = pk2h(z[6], z[7]);
;                     f16* dst = (br == 2) ? merged : Yb;
;                     gst16(dst + off + bj * HALF, w); } } } }
.LBB0_1243:
	s_mov_b32 s26, 0x8000
	v_cvt_pk_f16_f32 v154, v154, v155
	v_cvt_pk_f16_f32 v155, v158, v159
	v_add_co_u32_e32 v158, vcc, s26, v178
	v_cvt_pk_f16_f32 v156, v156, v157
	v_cvt_pk_f16_f32 v157, v160, v161
	v_addc_co_u32_e32 v159, vcc, 0, v179, vcc
	s_mov_b64 s[28:29], 0x800
	v_lshl_add_u64 v[222:223], v[224:225], 0, s[28:29]
	v_cndmask_b32_e64 v222, v158, v222, s[36:37]
	v_cndmask_b32_e64 v223, v159, v223, s[36:37]
	global_store_dwordx4 v[222:223], v[154:157], off
	v_cvt_f32_i32_e32 v150, v150
	v_cvt_f32_i32_e32 v151, v151
	v_cvt_f32_i32_e32 v154, v152
	v_cvt_f32_i32_e32 v152, v146
	v_cvt_f32_i32_e32 v156, v147
	v_mul_f32_e32 v146, v38, v150
	v_fma_f32 v146, v227, v146, v34
	v_mul_f32_e32 v147, v30, v152
	v_fma_f32 v147, v227, v147, v26
	v_exp_f32_e32 v147, v147
	v_exp_f32_e32 v146, v146
	v_cvt_f32_i32_e32 v155, v153
	v_add_f32_e32 v147, 1.0, v147
	v_rcp_f32_e32 v150, v147
	v_mul_f32_e32 v147, v39, v151
	v_fma_f32 v147, v227, v147, v35
	v_exp_f32_e32 v147, v147
	v_mul_f32_e32 v151, v31, v156
	v_fma_f32 v151, v227, v151, v27
	v_pk_add_f32 v[146:147], v[146:147], 1.0 op_sel_hi:[1,0]
	v_exp_f32_e32 v151, v151
	v_rcp_f32_e32 v146, v146
	v_rcp_f32_e32 v147, v147
	s_waitcnt vmcnt(3)
	v_cvt_f32_f16_sdwa v153, v162 dst_sel:DWORD dst_unused:UNUSED_PAD src0_sel:WORD_1
	v_cvt_f32_f16_e32 v152, v162
	v_add_f32_e32 v151, 1.0, v151
	v_rcp_f32_e32 v151, v151
	s_mov_b64 s[50:51], -1
	v_pk_mul_f32 v[146:147], v[146:147], v[152:153]
	v_cvt_f32_f16_sdwa v153, v164 dst_sel:DWORD dst_unused:UNUSED_PAD src0_sel:WORD_1
	v_cvt_f32_f16_e32 v152, v164
	s_and_b64 vcc, exec, s[38:39]
	v_pk_mul_f32 v[150:151], v[150:151], v[152:153]
	v_mul_f32_e32 v152, v40, v154
	v_mul_f32_e32 v153, v41, v155
	v_fma_f32 v152, v227, v152, v36
	v_fma_f32 v153, v227, v153, v37
	v_exp_f32_e32 v152, v152
	v_exp_f32_e32 v153, v153
	v_cvt_f32_f16_sdwa v155, v163 dst_sel:DWORD dst_unused:UNUSED_PAD src0_sel:WORD_1
	v_cvt_f32_f16_e32 v154, v163
	v_pk_add_f32 v[152:153], v[152:153], 1.0 op_sel_hi:[1,0]
	v_rcp_f32_e32 v152, v152
	v_rcp_f32_e32 v153, v153
	s_nop 0
	v_pk_mul_f32 v[152:153], v[152:153], v[154:155]
	s_cbranch_vccnz .LBB0_1245
	s_mov_b64 s[50:51], 0
.LBB0_1245:
	v_cvt_f32_i32_e32 v148, v148
	v_cvt_f32_i32_e32 v149, v149
	v_cvt_f32_f16_sdwa v155, v165 dst_sel:DWORD dst_unused:UNUSED_PAD src0_sel:WORD_1
	v_cvt_f32_f16_e32 v154, v165
	v_mul_f32_e32 v148, v32, v148
	v_mul_f32_e32 v149, v33, v149
	v_fma_f32 v148, v227, v148, v28
	v_fma_f32 v149, v227, v149, v29
	v_exp_f32_e32 v148, v148
	v_exp_f32_e32 v149, v149
	s_andn2_b64 vcc, exec, s[50:51]
	v_pk_add_f32 v[148:149], v[148:149], 1.0 op_sel_hi:[1,0]
	v_rcp_f32_e32 v148, v148
	v_rcp_f32_e32 v149, v149
	s_nop 0
	v_pk_mul_f32 v[148:149], v[148:149], v[154:155]
	s_cbranch_vccnz .LBB0_1247
	v_cvt_f32_f16_sdwa v155, v42 dst_sel:DWORD dst_unused:UNUSED_PAD src0_sel:WORD_1
	v_cvt_f32_f16_e32 v154, v42
	s_waitcnt vmcnt(1)
	v_cvt_f32_f16_sdwa v157, v46 dst_sel:DWORD dst_unused:UNUSED_PAD src0_sel:WORD_1
	v_cvt_f32_f16_e32 v156, v46
	v_cvt_f32_f16_sdwa v159, v43 dst_sel:DWORD dst_unused:UNUSED_PAD src0_sel:WORD_1
	v_cvt_f32_f16_e32 v158, v43
	v_cvt_f32_f16_sdwa v161, v47 dst_sel:DWORD dst_unused:UNUSED_PAD src0_sel:WORD_1
	v_cvt_f32_f16_e32 v160, v47
	v_cvt_f32_f16_sdwa v163, v44 dst_sel:DWORD dst_unused:UNUSED_PAD src0_sel:WORD_1
	v_cvt_f32_f16_e32 v162, v44
	v_cvt_f32_f16_sdwa v165, v48 dst_sel:DWORD dst_unused:UNUSED_PAD src0_sel:WORD_1
	v_cvt_f32_f16_e32 v164, v48
	v_cvt_f32_f16_sdwa v167, v45 dst_sel:DWORD dst_unused:UNUSED_PAD src0_sel:WORD_1
	v_cvt_f32_f16_e32 v166, v45
	v_cvt_f32_f16_sdwa v169, v49 dst_sel:DWORD dst_unused:UNUSED_PAD src0_sel:WORD_1
	v_cvt_f32_f16_e32 v168, v49
	v_pk_add_f32 v[154:155], v[156:157], v[154:155]
	v_pk_add_f32 v[156:157], v[160:161], v[158:159]
	v_pk_add_f32 v[158:159], v[164:165], v[162:163]
	v_pk_add_f32 v[160:161], v[168:169], v[166:167]
	v_pk_add_f32 v[146:147], v[146:147], v[154:155]
	v_pk_add_f32 v[152:153], v[152:153], v[156:157]
	v_pk_add_f32 v[150:151], v[150:151], v[158:159]
	v_pk_add_f32 v[148:149], v[148:149], v[160:161]

; __device__ __forceinline__ unsigned pk2h(float lo, float hi) { f32x2 v = {lo, hi}; f16x2 h = __builtin_convertvector(v, f16x2); return __builtin_bit_cast(unsigned, h); }
;     __device__ __forceinline__ void operator()(const f32x4 (&acc)[2][2][4][2], const Unit& u, int wr, int wc, int fr, int fq) const {
;     ...
;                 for (int bj = 0; bj < 2; ++bj) {
;                     f32x4 a0 = acc[ai][bj][m][0], a1 = acc[ai][bj][m][1];
;                     if constexpr (I8) { const i32x4 i0 = __builtin_bit_cast(i32x4, a0), i1 = __builtin_bit_cast(i32x4, a1);
;                         a0 = (f32x4){(float)i0.x, (float)i0.y, (float)i0.z, (float)i0.w} * sv[bj][0]; a1 = (f32x4){(float)i1.x, (float)i1.y, (float)i1.z, (float)i1.w} * sv[bj][1]; }
;                     const f32x4 g0 = a0 * rs[ai][m] + bv[bj][0], g1 = a1 * rs[ai][m] + bv[bj][1];
;                     const f16x8 yy = yv[m][bj];
;                     float z[8];
; #pragma unroll
;                     for (int e = 0; e < 4; ++e) { z[e] = (float)yy[e] * __builtin_amdgcn_rcpf(1.f + __builtin_amdgcn_exp2f(-LOG2E * g0[e])); z[4 + e] = (float)yy[4 + e] * __builtin_amdgcn_rcpf(1.f + __builtin_amdgcn_exp2f(-LOG2E * g1[e])); }
;                     if (br == 2) {
; #pragma unroll
;                         for (int e = 0; e < 8; ++e) z[e] += (float)za[bj][e] + (float)zb[bj][e]; }
;                     u32x4 w; w.x = pk2h(z[0], z[1]); w.y = pk2h(z[2], z[3]); w.z = pk2h(z[4], z[5]); w.w = pk2h(z[6], z[7]);
;                     f16* dst = (br == 2) ? merged : Yb;
;                     gst16(dst + off + bj * HALF, w); } } } }
.LBB0_1249:
	v_cvt_f32_i32_e32 v162, v138
	v_cvt_f32_i32_e32 v163, v139
	v_cvt_f32_i32_e32 v142, v142
	v_cvt_f32_i32_e32 v143, v143
	v_mul_f32_e32 v139, v54, v162
	v_fma_f32 v139, v220, v139, v50
	v_exp_f32_e32 v139, v139
	v_cvt_f32_i32_e32 v164, v140
	v_mul_f32_e32 v138, v70, v142
	v_fma_f32 v138, v220, v138, v62
	v_add_f32_e32 v139, 1.0, v139
	v_rcp_f32_e32 v140, v139
	v_mul_f32_e32 v139, v71, v143
	v_fma_f32 v139, v220, v139, v63
	v_exp_f32_e32 v138, v138
	v_exp_f32_e32 v139, v139
	v_cvt_f32_i32_e32 v165, v141
	v_mul_f32_e32 v141, v55, v163
	v_fma_f32 v141, v220, v141, v51
	v_pk_add_f32 v[138:139], v[138:139], 1.0 op_sel_hi:[1,0]
	v_exp_f32_e32 v141, v141
	v_rcp_f32_e32 v138, v138
	v_rcp_f32_e32 v139, v139
	s_waitcnt vmcnt(3)
	v_cvt_f32_f16_sdwa v143, v158 dst_sel:DWORD dst_unused:UNUSED_PAD src0_sel:WORD_1
	v_cvt_f32_f16_e32 v142, v158
	v_add_f32_e32 v141, 1.0, v141
	v_rcp_f32_e32 v141, v141
	v_cvt_f32_i32_e32 v144, v144
	v_pk_mul_f32 v[138:139], v[138:139], v[142:143]
	v_cvt_f32_f16_sdwa v143, v160 dst_sel:DWORD dst_unused:UNUSED_PAD src0_sel:WORD_1
	v_cvt_f32_f16_e32 v142, v160
	v_cvt_f32_i32_e32 v145, v145
	v_cvt_f32_f16_sdwa v163, v159 dst_sel:DWORD dst_unused:UNUSED_PAD src0_sel:WORD_1
	v_cvt_f32_f16_e32 v162, v159
	v_pk_mul_f32 v[140:141], v[140:141], v[142:143]
	v_mul_f32_e32 v143, v56, v164
	v_fma_f32 v143, v220, v143, v52
	v_exp_f32_e32 v143, v143
	v_mul_f32_e32 v142, v72, v144
	v_fma_f32 v142, v220, v142, v64
	v_add_f32_e32 v143, 1.0, v143
	v_rcp_f32_e32 v144, v143
	v_mul_f32_e32 v143, v73, v145
	v_mul_f32_e32 v145, v57, v165
	v_fma_f32 v143, v220, v143, v65
	v_fma_f32 v145, v220, v145, v53
	v_exp_f32_e32 v142, v142
	v_exp_f32_e32 v143, v143
	v_exp_f32_e32 v145, v145
	v_cvt_f32_f16_sdwa v159, v161 dst_sel:DWORD dst_unused:UNUSED_PAD src0_sel:WORD_1
	v_pk_add_f32 v[142:143], v[142:143], 1.0 op_sel_hi:[1,0]
	v_add_f32_e32 v145, 1.0, v145
	v_rcp_f32_e32 v142, v142
	v_rcp_f32_e32 v143, v143
	v_rcp_f32_e32 v145, v145
	v_cvt_f32_f16_e32 v158, v161
	s_and_b64 vcc, exec, s[36:37]
	v_pk_mul_f32 v[142:143], v[142:143], v[162:163]
	v_pk_mul_f32 v[144:145], v[144:145], v[158:159]
	s_cbranch_vccnz .LBB0_1251
	v_cvt_f32_f16_sdwa v159, v58 dst_sel:DWORD dst_unused:UNUSED_PAD src0_sel:WORD_1
	v_cvt_f32_f16_e32 v158, v58
	s_waitcnt vmcnt(1)
	v_cvt_f32_f16_sdwa v161, v66 dst_sel:DWORD dst_unused:UNUSED_PAD src0_sel:WORD_1
	v_cvt_f32_f16_e32 v160, v66
	v_cvt_f32_f16_sdwa v163, v59 dst_sel:DWORD dst_unused:UNUSED_PAD src0_sel:WORD_1
	v_cvt_f32_f16_e32 v162, v59
	v_cvt_f32_f16_sdwa v165, v67 dst_sel:DWORD dst_unused:UNUSED_PAD src0_sel:WORD_1
	v_cvt_f32_f16_e32 v164, v67
	v_cvt_f32_f16_sdwa v167, v60 dst_sel:DWORD dst_unused:UNUSED_PAD src0_sel:WORD_1
	v_cvt_f32_f16_e32 v166, v60
	v_cvt_f32_f16_sdwa v169, v68 dst_sel:DWORD dst_unused:UNUSED_PAD src0_sel:WORD_1
	v_cvt_f32_f16_e32 v168, v68
	v_cvt_f32_f16_sdwa v171, v61 dst_sel:DWORD dst_unused:UNUSED_PAD src0_sel:WORD_1
	v_cvt_f32_f16_e32 v170, v61
	v_cvt_f32_f16_sdwa v173, v69 dst_sel:DWORD dst_unused:UNUSED_PAD src0_sel:WORD_1
	v_cvt_f32_f16_e32 v172, v69
	v_pk_add_f32 v[158:159], v[160:161], v[158:159]
	v_pk_add_f32 v[160:161], v[164:165], v[162:163]
	v_pk_add_f32 v[162:163], v[168:169], v[166:167]
	v_pk_add_f32 v[164:165], v[172:173], v[170:171]
	v_pk_add_f32 v[138:139], v[138:139], v[158:159]
	v_pk_add_f32 v[142:143], v[142:143], v[160:161]
	v_pk_add_f32 v[140:141], v[140:141], v[162:163]
	v_pk_add_f32 v[144:145], v[144:145], v[164:165]
; __device__ __forceinline__ unsigned pk2h(float lo, float hi) { f32x2 v = {lo, hi}; f16x2 h = __builtin_convertvector(v, f16x2); return __builtin_bit_cast(unsigned, h); }
;     __device__ __forceinline__ void operator()(const f32x4 (&acc)[2][2][4][2], const Unit& u, int wr, int wc, int fr, int fq) const {
;     ...
;                 for (int bj = 0; bj < 2; ++bj) {
;                     f32x4 a0 = acc[ai][bj][m][0], a1 = acc[ai][bj][m][1];
;                     if constexpr (I8) { const i32x4 i0 = __builtin_bit_cast(i32x4, a0), i1 = __builtin_bit_cast(i32x4, a1);
;                         a0 = (f32x4){(float)i0.x, (float)i0.y, (float)i0.z, (float)i0.w} * sv[bj][0]; a1 = (f32x4){(float)i1.x, (float)i1.y, (float)i1.z, (float)i1.w} * sv[bj][1]; }
;                     const f32x4 g0 = a0 * rs[ai][m] + bv[bj][0], g1 = a1 * rs[ai][m] + bv[bj][1];
;                     const f16x8 yy = yv[m][bj];
;                     float z[8];
; #pragma unroll
;                     for (int e = 0; e < 4; ++e) { z[e] = (float)yy[e] * __builtin_amdgcn_rcpf(1.f + __builtin_amdgcn_exp2f(-LOG2E * g0[e])); z[4 + e] = (float)yy[4 + e] * __builtin_amdgcn_rcpf(1.f + __builtin_amdgcn_exp2f(-LOG2E * g1[e])); }
;                     if (br == 2) {
; #pragma unroll
;                         for (int e = 0; e < 8; ++e) z[e] += (float)za[bj][e] + (float)zb[bj][e]; }
;                     u32x4 w; w.x = pk2h(z[0], z[1]); w.y = pk2h(z[2], z[3]); w.z = pk2h(z[4], z[5]); w.w = pk2h(z[6], z[7]);
;                     f16* dst = (br == 2) ? merged : Yb;
;                     gst16(dst + off + bj * HALF, w); } } } }
.LBB0_1251:
	s_mov_b32 s26, 0x10000
	v_cvt_pk_f16_f32 v138, v138, v139
	v_cvt_pk_f16_f32 v139, v142, v143
	v_add_co_u32_e32 v142, vcc, s26, v178
	v_cvt_pk_f16_f32 v140, v140, v141
	v_cvt_pk_f16_f32 v141, v144, v145
	v_addc_co_u32_e32 v143, vcc, 0, v179, vcc
	s_mov_b64 s[28:29], 0x1000
	v_lshl_add_u64 v[222:223], v[224:225], 0, s[28:29]
	v_cndmask_b32_e64 v222, v142, v222, s[36:37]
	v_cndmask_b32_e64 v223, v143, v223, s[36:37]
	global_store_dwordx4 v[222:223], v[138:141], off
	v_cvt_f32_i32_e32 v134, v134
	v_cvt_f32_i32_e32 v135, v135
	v_cvt_f32_i32_e32 v138, v136
	v_cvt_f32_i32_e32 v136, v130
	v_cvt_f32_i32_e32 v140, v131
	v_mul_f32_e32 v130, v38, v134
	v_fma_f32 v130, v220, v130, v34
	v_mul_f32_e32 v131, v30, v136
	v_fma_f32 v131, v220, v131, v26
	v_exp_f32_e32 v131, v131
	v_exp_f32_e32 v130, v130
	v_cvt_f32_i32_e32 v139, v137
	v_add_f32_e32 v131, 1.0, v131
	v_rcp_f32_e32 v134, v131
	v_mul_f32_e32 v131, v39, v135
	v_fma_f32 v131, v220, v131, v35
	v_exp_f32_e32 v131, v131
	v_mul_f32_e32 v135, v31, v140
	v_fma_f32 v135, v220, v135, v27
	v_pk_add_f32 v[130:131], v[130:131], 1.0 op_sel_hi:[1,0]
	v_exp_f32_e32 v135, v135
	v_rcp_f32_e32 v130, v130
	v_rcp_f32_e32 v131, v131
	s_waitcnt vmcnt(3)
	v_cvt_f32_f16_sdwa v137, v154 dst_sel:DWORD dst_unused:UNUSED_PAD src0_sel:WORD_1
	v_cvt_f32_f16_e32 v136, v154
	v_add_f32_e32 v135, 1.0, v135
	v_rcp_f32_e32 v135, v135
	s_mov_b64 s[50:51], -1
	v_pk_mul_f32 v[130:131], v[130:131], v[136:137]
	v_cvt_f32_f16_sdwa v137, v156 dst_sel:DWORD dst_unused:UNUSED_PAD src0_sel:WORD_1
	v_cvt_f32_f16_e32 v136, v156
	s_and_b64 vcc, exec, s[38:39]
	v_pk_mul_f32 v[134:135], v[134:135], v[136:137]
	v_mul_f32_e32 v136, v40, v138
	v_mul_f32_e32 v137, v41, v139
	v_fma_f32 v136, v220, v136, v36
	v_fma_f32 v137, v220, v137, v37
	v_exp_f32_e32 v136, v136
	v_exp_f32_e32 v137, v137
	v_cvt_f32_f16_sdwa v139, v155 dst_sel:DWORD dst_unused:UNUSED_PAD src0_sel:WORD_1
	v_cvt_f32_f16_e32 v138, v155
	v_pk_add_f32 v[136:137], v[136:137], 1.0 op_sel_hi:[1,0]
	v_rcp_f32_e32 v136, v136
	v_rcp_f32_e32 v137, v137
	s_nop 0
	v_pk_mul_f32 v[136:137], v[136:137], v[138:139]
	s_cbranch_vccnz .LBB0_1253
	s_mov_b64 s[50:51], 0
.LBB0_1253:
	v_cvt_f32_i32_e32 v132, v132
	v_cvt_f32_i32_e32 v133, v133
	v_cvt_f32_f16_sdwa v139, v157 dst_sel:DWORD dst_unused:UNUSED_PAD src0_sel:WORD_1
	v_cvt_f32_f16_e32 v138, v157
	v_mul_f32_e32 v132, v32, v132
	v_mul_f32_e32 v133, v33, v133
	v_fma_f32 v132, v220, v132, v28
	v_fma_f32 v133, v220, v133, v29
	v_exp_f32_e32 v132, v132
	v_exp_f32_e32 v133, v133
	s_andn2_b64 vcc, exec, s[50:51]
	v_pk_add_f32 v[132:133], v[132:133], 1.0 op_sel_hi:[1,0]
	v_rcp_f32_e32 v132, v132
	v_rcp_f32_e32 v133, v133
	s_nop 0
	v_pk_mul_f32 v[132:133], v[132:133], v[138:139]
	s_cbranch_vccnz .LBB0_1255
	v_cvt_f32_f16_sdwa v139, v42 dst_sel:DWORD dst_unused:UNUSED_PAD src0_sel:WORD_1
	v_cvt_f32_f16_e32 v138, v42
	s_waitcnt vmcnt(1)
	v_cvt_f32_f16_sdwa v141, v46 dst_sel:DWORD dst_unused:UNUSED_PAD src0_sel:WORD_1
	v_cvt_f32_f16_e32 v140, v46
	v_cvt_f32_f16_sdwa v143, v43 dst_sel:DWORD dst_unused:UNUSED_PAD src0_sel:WORD_1
	v_cvt_f32_f16_e32 v142, v43
	v_cvt_f32_f16_sdwa v145, v47 dst_sel:DWORD dst_unused:UNUSED_PAD src0_sel:WORD_1
	v_cvt_f32_f16_e32 v144, v47
	v_cvt_f32_f16_sdwa v155, v44 dst_sel:DWORD dst_unused:UNUSED_PAD src0_sel:WORD_1
	v_cvt_f32_f16_e32 v154, v44
	v_cvt_f32_f16_sdwa v157, v48 dst_sel:DWORD dst_unused:UNUSED_PAD src0_sel:WORD_1
	v_cvt_f32_f16_e32 v156, v48
	v_cvt_f32_f16_sdwa v159, v45 dst_sel:DWORD dst_unused:UNUSED_PAD src0_sel:WORD_1
	v_cvt_f32_f16_e32 v158, v45
	v_cvt_f32_f16_sdwa v161, v49 dst_sel:DWORD dst_unused:UNUSED_PAD src0_sel:WORD_1
	v_cvt_f32_f16_e32 v160, v49
	v_pk_add_f32 v[138:139], v[140:141], v[138:139]
	v_pk_add_f32 v[140:141], v[144:145], v[142:143]
	v_pk_add_f32 v[142:143], v[156:157], v[154:155]
	v_pk_add_f32 v[144:145], v[160:161], v[158:159]
	v_pk_add_f32 v[130:131], v[130:131], v[138:139]
	v_pk_add_f32 v[136:137], v[136:137], v[140:141]
	v_pk_add_f32 v[134:135], v[134:135], v[142:143]
	v_pk_add_f32 v[132:133], v[132:133], v[144:145]

; __device__ __forceinline__ unsigned pk2h(float lo, float hi) { f32x2 v = {lo, hi}; f16x2 h = __builtin_convertvector(v, f16x2); return __builtin_bit_cast(unsigned, h); }
;     __device__ __forceinline__ void operator()(const f32x4 (&acc)[2][2][4][2], const Unit& u, int wr, int wc, int fr, int fq) const {
;     ...
;                 for (int bj = 0; bj < 2; ++bj) {
;                     f32x4 a0 = acc[ai][bj][m][0], a1 = acc[ai][bj][m][1];
;                     if constexpr (I8) { const i32x4 i0 = __builtin_bit_cast(i32x4, a0), i1 = __builtin_bit_cast(i32x4, a1);
;                         a0 = (f32x4){(float)i0.x, (float)i0.y, (float)i0.z, (float)i0.w} * sv[bj][0]; a1 = (f32x4){(float)i1.x, (float)i1.y, (float)i1.z, (float)i1.w} * sv[bj][1]; }
;                     const f32x4 g0 = a0 * rs[ai][m] + bv[bj][0], g1 = a1 * rs[ai][m] + bv[bj][1];
;                     const f16x8 yy = yv[m][bj];
;                     float z[8];
; #pragma unroll
;                     for (int e = 0; e < 4; ++e) { z[e] = (float)yy[e] * __builtin_amdgcn_rcpf(1.f + __builtin_amdgcn_exp2f(-LOG2E * g0[e])); z[4 + e] = (float)yy[4 + e] * __builtin_amdgcn_rcpf(1.f + __builtin_amdgcn_exp2f(-LOG2E * g1[e])); }
;                     if (br == 2) {
; #pragma unroll
;                         for (int e = 0; e < 8; ++e) z[e] += (float)za[bj][e] + (float)zb[bj][e]; }
;                     u32x4 w; w.x = pk2h(z[0], z[1]); w.y = pk2h(z[2], z[3]); w.z = pk2h(z[4], z[5]); w.w = pk2h(z[6], z[7]);
;                     f16* dst = (br == 2) ? merged : Yb;
;                     gst16(dst + off + bj * HALF, w); } } } }
.LBB0_1257:
	v_cvt_f32_i32_e32 v130, v122
	v_cvt_f32_i32_e32 v131, v123
	v_cvt_f32_i32_e32 v126, v126
	v_cvt_f32_i32_e32 v127, v127
	v_mul_f32_e32 v123, v54, v130
	v_fma_f32 v123, v221, v123, v50
	v_exp_f32_e32 v123, v123
	v_cvt_f32_i32_e32 v132, v124
	v_mul_f32_e32 v122, v70, v126
	v_fma_f32 v122, v221, v122, v62
	v_add_f32_e32 v123, 1.0, v123
	v_rcp_f32_e32 v124, v123
	v_mul_f32_e32 v123, v71, v127
	v_fma_f32 v123, v221, v123, v63
	v_exp_f32_e32 v122, v122
	v_exp_f32_e32 v123, v123
	v_cvt_f32_i32_e32 v133, v125
	v_mul_f32_e32 v125, v55, v131
	v_fma_f32 v125, v221, v125, v51
	v_pk_add_f32 v[122:123], v[122:123], 1.0 op_sel_hi:[1,0]
	v_exp_f32_e32 v125, v125
	v_rcp_f32_e32 v122, v122
	v_rcp_f32_e32 v123, v123
	s_waitcnt vmcnt(3)
	v_cvt_f32_f16_sdwa v127, v150 dst_sel:DWORD dst_unused:UNUSED_PAD src0_sel:WORD_1
	v_cvt_f32_f16_e32 v126, v150
	v_add_f32_e32 v125, 1.0, v125
	v_rcp_f32_e32 v125, v125
	v_cvt_f32_i32_e32 v128, v128
	v_pk_mul_f32 v[122:123], v[122:123], v[126:127]
	v_cvt_f32_f16_sdwa v127, v152 dst_sel:DWORD dst_unused:UNUSED_PAD src0_sel:WORD_1
	v_cvt_f32_f16_e32 v126, v152
	v_cvt_f32_i32_e32 v129, v129
	v_cvt_f32_f16_sdwa v131, v151 dst_sel:DWORD dst_unused:UNUSED_PAD src0_sel:WORD_1
	v_cvt_f32_f16_e32 v130, v151
	v_pk_mul_f32 v[124:125], v[124:125], v[126:127]
	v_mul_f32_e32 v127, v56, v132
	v_fma_f32 v127, v221, v127, v52
	v_exp_f32_e32 v127, v127
	v_mul_f32_e32 v126, v72, v128
	v_fma_f32 v126, v221, v126, v64
	v_add_f32_e32 v127, 1.0, v127
	v_rcp_f32_e32 v128, v127
	v_mul_f32_e32 v127, v73, v129
	v_fma_f32 v127, v221, v127, v65
	v_exp_f32_e32 v126, v126
	v_exp_f32_e32 v127, v127
	v_mul_f32_e32 v129, v57, v133
	v_fma_f32 v129, v221, v129, v53
	v_pk_add_f32 v[126:127], v[126:127], 1.0 op_sel_hi:[1,0]
	v_exp_f32_e32 v129, v129
	v_rcp_f32_e32 v126, v126
	v_rcp_f32_e32 v127, v127
	s_and_b64 vcc, exec, s[36:37]
	v_add_f32_e32 v129, 1.0, v129
	v_rcp_f32_e32 v129, v129
	v_pk_mul_f32 v[126:127], v[126:127], v[130:131]
	v_cvt_f32_f16_sdwa v131, v153 dst_sel:DWORD dst_unused:UNUSED_PAD src0_sel:WORD_1
	v_cvt_f32_f16_e32 v130, v153
	v_pk_mul_f32 v[128:129], v[128:129], v[130:131]
	s_cbranch_vccnz .LBB0_1259
	v_cvt_f32_f16_sdwa v131, v58 dst_sel:DWORD dst_unused:UNUSED_PAD src0_sel:WORD_1
	v_cvt_f32_f16_e32 v130, v58
	s_waitcnt vmcnt(1)
	v_cvt_f32_f16_sdwa v133, v66 dst_sel:DWORD dst_unused:UNUSED_PAD src0_sel:WORD_1
	v_cvt_f32_f16_e32 v132, v66
	v_cvt_f32_f16_sdwa v135, v59 dst_sel:DWORD dst_unused:UNUSED_PAD src0_sel:WORD_1
	v_cvt_f32_f16_e32 v134, v59
	v_cvt_f32_f16_sdwa v137, v67 dst_sel:DWORD dst_unused:UNUSED_PAD src0_sel:WORD_1
	v_cvt_f32_f16_e32 v136, v67
	v_cvt_f32_f16_sdwa v139, v60 dst_sel:DWORD dst_unused:UNUSED_PAD src0_sel:WORD_1
	v_cvt_f32_f16_e32 v138, v60
	v_cvt_f32_f16_sdwa v141, v68 dst_sel:DWORD dst_unused:UNUSED_PAD src0_sel:WORD_1
	v_cvt_f32_f16_e32 v140, v68
	v_cvt_f32_f16_sdwa v143, v61 dst_sel:DWORD dst_unused:UNUSED_PAD src0_sel:WORD_1
	v_cvt_f32_f16_e32 v142, v61
	v_cvt_f32_f16_sdwa v145, v69 dst_sel:DWORD dst_unused:UNUSED_PAD src0_sel:WORD_1
	v_cvt_f32_f16_e32 v144, v69
	v_pk_add_f32 v[130:131], v[132:133], v[130:131]
	v_pk_add_f32 v[132:133], v[136:137], v[134:135]
	v_pk_add_f32 v[134:135], v[140:141], v[138:139]
	v_pk_add_f32 v[136:137], v[144:145], v[142:143]
	v_pk_add_f32 v[122:123], v[122:123], v[130:131]
	v_pk_add_f32 v[126:127], v[126:127], v[132:133]
	v_pk_add_f32 v[124:125], v[124:125], v[134:135]
	v_pk_add_f32 v[128:129], v[128:129], v[136:137]
; __device__ __forceinline__ unsigned pk2h(float lo, float hi) { f32x2 v = {lo, hi}; f16x2 h = __builtin_convertvector(v, f16x2); return __builtin_bit_cast(unsigned, h); }
;     __device__ __forceinline__ void operator()(const f32x4 (&acc)[2][2][4][2], const Unit& u, int wr, int wc, int fr, int fq) const {
;     ...
;                 for (int bj = 0; bj < 2; ++bj) {
;                     f32x4 a0 = acc[ai][bj][m][0], a1 = acc[ai][bj][m][1];
;                     if constexpr (I8) { const i32x4 i0 = __builtin_bit_cast(i32x4, a0), i1 = __builtin_bit_cast(i32x4, a1);
;                         a0 = (f32x4){(float)i0.x, (float)i0.y, (float)i0.z, (float)i0.w} * sv[bj][0]; a1 = (f32x4){(float)i1.x, (float)i1.y, (float)i1.z, (float)i1.w} * sv[bj][1]; }
;                     const f32x4 g0 = a0 * rs[ai][m] + bv[bj][0], g1 = a1 * rs[ai][m] + bv[bj][1];
;                     const f16x8 yy = yv[m][bj];
;                     float z[8];
; #pragma unroll
;                     for (int e = 0; e < 4; ++e) { z[e] = (float)yy[e] * __builtin_amdgcn_rcpf(1.f + __builtin_amdgcn_exp2f(-LOG2E * g0[e])); z[4 + e] = (float)yy[4 + e] * __builtin_amdgcn_rcpf(1.f + __builtin_amdgcn_exp2f(-LOG2E * g1[e])); }
;                     if (br == 2) {
; #pragma unroll
;                         for (int e = 0; e < 8; ++e) z[e] += (float)za[bj][e] + (float)zb[bj][e]; }
;                     u32x4 w; w.x = pk2h(z[0], z[1]); w.y = pk2h(z[2], z[3]); w.z = pk2h(z[4], z[5]); w.w = pk2h(z[6], z[7]);
;                     f16* dst = (br == 2) ? merged : Yb;
;                     gst16(dst + off + bj * HALF, w); } } } }
.LBB0_1259:
	s_mov_b32 s26, 0x18000
	v_cvt_pk_f16_f32 v122, v122, v123
	v_cvt_pk_f16_f32 v123, v126, v127
	v_add_co_u32_e32 v126, vcc, s26, v178
	v_cvt_pk_f16_f32 v124, v124, v125
	v_cvt_pk_f16_f32 v125, v128, v129
	v_addc_co_u32_e32 v127, vcc, 0, v179, vcc
	s_mov_b64 s[28:29], 0x1800
	v_lshl_add_u64 v[222:223], v[224:225], 0, s[28:29]
	v_cndmask_b32_e64 v222, v126, v222, s[36:37]
	v_cndmask_b32_e64 v223, v127, v223, s[36:37]
	global_store_dwordx4 v[222:223], v[122:125], off
	v_cvt_f32_i32_e32 v118, v118
	v_cvt_f32_i32_e32 v119, v119
	v_cvt_f32_i32_e32 v122, v120
	v_cvt_f32_i32_e32 v120, v114
	v_cvt_f32_i32_e32 v124, v115
	v_mul_f32_e32 v114, v38, v118
	v_fma_f32 v114, v221, v114, v34
	v_mul_f32_e32 v115, v30, v120
	v_fma_f32 v115, v221, v115, v26
	v_exp_f32_e32 v115, v115
	v_exp_f32_e32 v114, v114
	v_cvt_f32_i32_e32 v123, v121
	v_add_f32_e32 v115, 1.0, v115
	v_rcp_f32_e32 v118, v115
	v_mul_f32_e32 v115, v39, v119
	v_fma_f32 v115, v221, v115, v35
	v_exp_f32_e32 v115, v115
	v_mul_f32_e32 v119, v31, v124
	v_fma_f32 v119, v221, v119, v27
	v_pk_add_f32 v[114:115], v[114:115], 1.0 op_sel_hi:[1,0]
	v_exp_f32_e32 v119, v119
	v_rcp_f32_e32 v114, v114
	v_rcp_f32_e32 v115, v115
	s_waitcnt vmcnt(3)
	v_cvt_f32_f16_sdwa v121, v146 dst_sel:DWORD dst_unused:UNUSED_PAD src0_sel:WORD_1
	v_cvt_f32_f16_e32 v120, v146
	v_add_f32_e32 v119, 1.0, v119
	v_rcp_f32_e32 v119, v119
	s_mov_b64 s[50:51], -1
	v_pk_mul_f32 v[114:115], v[114:115], v[120:121]
	v_cvt_f32_f16_sdwa v121, v148 dst_sel:DWORD dst_unused:UNUSED_PAD src0_sel:WORD_1
	v_cvt_f32_f16_e32 v120, v148
	s_and_b64 vcc, exec, s[38:39]
	v_pk_mul_f32 v[118:119], v[118:119], v[120:121]
	v_mul_f32_e32 v120, v40, v122
	v_mul_f32_e32 v121, v41, v123
	v_fma_f32 v120, v221, v120, v36
	v_fma_f32 v121, v221, v121, v37
	v_exp_f32_e32 v120, v120
	v_exp_f32_e32 v121, v121
	v_cvt_f32_f16_sdwa v123, v147 dst_sel:DWORD dst_unused:UNUSED_PAD src0_sel:WORD_1
	v_cvt_f32_f16_e32 v122, v147
	v_pk_add_f32 v[120:121], v[120:121], 1.0 op_sel_hi:[1,0]
	v_rcp_f32_e32 v120, v120
	v_rcp_f32_e32 v121, v121
	s_nop 0
	v_pk_mul_f32 v[120:121], v[120:121], v[122:123]
	s_cbranch_vccnz .LBB0_1261
	s_mov_b64 s[50:51], 0
.LBB0_1261:
	v_cvt_f32_i32_e32 v116, v116
	v_cvt_f32_i32_e32 v117, v117
	v_cvt_f32_f16_sdwa v123, v149 dst_sel:DWORD dst_unused:UNUSED_PAD src0_sel:WORD_1
	v_cvt_f32_f16_e32 v122, v149
	v_mul_f32_e32 v116, v32, v116
	v_mul_f32_e32 v117, v33, v117
	v_fma_f32 v116, v221, v116, v28
	v_fma_f32 v117, v221, v117, v29
	v_exp_f32_e32 v116, v116
	v_exp_f32_e32 v117, v117
	s_andn2_b64 vcc, exec, s[50:51]
	v_pk_add_f32 v[116:117], v[116:117], 1.0 op_sel_hi:[1,0]
	v_rcp_f32_e32 v116, v116
	v_rcp_f32_e32 v117, v117
	s_nop 0
	v_pk_mul_f32 v[116:117], v[116:117], v[122:123]
	s_cbranch_vccnz .LBB0_1263
	v_cvt_f32_f16_sdwa v123, v42 dst_sel:DWORD dst_unused:UNUSED_PAD src0_sel:WORD_1
	v_cvt_f32_f16_e32 v122, v42
	s_waitcnt vmcnt(1)
	v_cvt_f32_f16_sdwa v125, v46 dst_sel:DWORD dst_unused:UNUSED_PAD src0_sel:WORD_1
	v_cvt_f32_f16_e32 v124, v46
	v_cvt_f32_f16_sdwa v127, v43 dst_sel:DWORD dst_unused:UNUSED_PAD src0_sel:WORD_1
	v_cvt_f32_f16_e32 v126, v43
	v_cvt_f32_f16_sdwa v129, v47 dst_sel:DWORD dst_unused:UNUSED_PAD src0_sel:WORD_1
	v_cvt_f32_f16_e32 v128, v47
	v_cvt_f32_f16_sdwa v131, v44 dst_sel:DWORD dst_unused:UNUSED_PAD src0_sel:WORD_1
	v_cvt_f32_f16_e32 v130, v44
	v_cvt_f32_f16_sdwa v133, v48 dst_sel:DWORD dst_unused:UNUSED_PAD src0_sel:WORD_1
	v_cvt_f32_f16_e32 v132, v48
	v_cvt_f32_f16_sdwa v135, v45 dst_sel:DWORD dst_unused:UNUSED_PAD src0_sel:WORD_1
	v_cvt_f32_f16_e32 v134, v45
	v_cvt_f32_f16_sdwa v137, v49 dst_sel:DWORD dst_unused:UNUSED_PAD src0_sel:WORD_1
	v_cvt_f32_f16_e32 v136, v49
	v_pk_add_f32 v[122:123], v[124:125], v[122:123]
	v_pk_add_f32 v[124:125], v[128:129], v[126:127]
	v_pk_add_f32 v[126:127], v[132:133], v[130:131]
	v_pk_add_f32 v[128:129], v[136:137], v[134:135]
	v_pk_add_f32 v[114:115], v[114:115], v[122:123]
	v_pk_add_f32 v[120:121], v[120:121], v[124:125]
	v_pk_add_f32 v[118:119], v[118:119], v[126:127]
	v_pk_add_f32 v[116:117], v[116:117], v[128:129]

;     __device__ __forceinline__ void operator()(const f32x4 (&acc)[2][2][4][2], const Unit& u, int wr, int wc, int fr, int fq) const {
;     ...
;                 for (int bj = 0; bj < 2; ++bj) {
;                     f32x4 a0 = acc[ai][bj][m][0], a1 = acc[ai][bj][m][1];
;                     if constexpr (I8) { const i32x4 i0 = __builtin_bit_cast(i32x4, a0), i1 = __builtin_bit_cast(i32x4, a1);
;                         a0 = (f32x4){(float)i0.x, (float)i0.y, (float)i0.z, (float)i0.w} * sv[bj][0]; a1 = (f32x4){(float)i1.x, (float)i1.y, (float)i1.z, (float)i1.w} * sv[bj][1]; }
;                     const f32x4 g0 = a0 * rs[ai][m] + bv[bj][0], g1 = a1 * rs[ai][m] + bv[bj][1];
;                     const f16x8 yy = yv[m][bj];
;                     float z[8];
; #pragma unroll
;                     for (int e = 0; e < 4; ++e) { z[e] = (float)yy[e] * __builtin_amdgcn_rcpf(1.f + __builtin_amdgcn_exp2f(-LOG2E * g0[e])); z[4 + e] = (float)yy[4 + e] * __builtin_amdgcn_rcpf(1.f + __builtin_amdgcn_exp2f(-LOG2E * g1[e])); }
;                     if (br == 2) {
; #pragma unroll
;                         for (int e = 0; e < 8; ++e) z[e] += (float)za[bj][e] + (float)zb[bj][e]; }
.LBB0_1265:
	v_cvt_f32_i32_e32 v134, v106
	v_cvt_f32_i32_e32 v135, v107
	v_cvt_f32_i32_e32 v110, v110
	v_cvt_f32_i32_e32 v111, v111
	v_mul_f32_e32 v107, v54, v134
	v_fma_f32 v107, v214, v107, v50
	v_exp_f32_e32 v107, v107
	v_cvt_f32_i32_e32 v136, v108
	v_mul_f32_e32 v106, v70, v110
	v_fma_f32 v106, v214, v106, v62
	v_add_f32_e32 v107, 1.0, v107
	v_rcp_f32_e32 v108, v107
	v_mul_f32_e32 v107, v71, v111
	v_fma_f32 v107, v214, v107, v63
	v_exp_f32_e32 v106, v106
	v_exp_f32_e32 v107, v107
	v_cvt_f32_i32_e32 v137, v109
	v_mul_f32_e32 v109, v55, v135
	v_fma_f32 v109, v214, v109, v51
	v_pk_add_f32 v[106:107], v[106:107], 1.0 op_sel_hi:[1,0]
	v_exp_f32_e32 v109, v109
	v_rcp_f32_e32 v106, v106
	v_rcp_f32_e32 v107, v107
	s_waitcnt vmcnt(3)
	v_cvt_f32_f16_sdwa v111, v126 dst_sel:DWORD dst_unused:UNUSED_PAD src0_sel:WORD_1
	v_cvt_f32_f16_e32 v110, v126
	v_add_f32_e32 v109, 1.0, v109
	v_rcp_f32_e32 v109, v109
	v_cvt_f32_i32_e32 v112, v112
	v_pk_mul_f32 v[106:107], v[106:107], v[110:111]
	v_cvt_f32_f16_sdwa v111, v128 dst_sel:DWORD dst_unused:UNUSED_PAD src0_sel:WORD_1
	v_cvt_f32_f16_e32 v110, v128
	v_cvt_f32_i32_e32 v113, v113
	v_cvt_f32_f16_sdwa v135, v127 dst_sel:DWORD dst_unused:UNUSED_PAD src0_sel:WORD_1
	v_cvt_f32_f16_e32 v134, v127
	v_pk_mul_f32 v[108:109], v[108:109], v[110:111]
	v_mul_f32_e32 v111, v56, v136
	v_fma_f32 v111, v214, v111, v52
	v_exp_f32_e32 v111, v111
	v_mul_f32_e32 v110, v72, v112
	v_fma_f32 v110, v214, v110, v64
	v_add_f32_e32 v111, 1.0, v111
	v_rcp_f32_e32 v112, v111
	v_mul_f32_e32 v111, v73, v113
	v_mul_f32_e32 v113, v57, v137
	v_fma_f32 v111, v214, v111, v65
	v_fma_f32 v113, v214, v113, v53
	v_exp_f32_e32 v110, v110
	v_exp_f32_e32 v111, v111
	v_exp_f32_e32 v113, v113
	v_cvt_f32_f16_sdwa v127, v129 dst_sel:DWORD dst_unused:UNUSED_PAD src0_sel:WORD_1
	v_pk_add_f32 v[110:111], v[110:111], 1.0 op_sel_hi:[1,0]
	v_add_f32_e32 v113, 1.0, v113
	v_rcp_f32_e32 v110, v110
	v_rcp_f32_e32 v111, v111
	v_rcp_f32_e32 v113, v113
	v_cvt_f32_f16_e32 v126, v129
	s_and_b64 vcc, exec, s[36:37]
	v_pk_mul_f32 v[110:111], v[110:111], v[134:135]
	v_pk_mul_f32 v[112:113], v[112:113], v[126:127]
	s_cbranch_vccnz .LBB0_1267
	v_cvt_f32_f16_sdwa v127, v58 dst_sel:DWORD dst_unused:UNUSED_PAD src0_sel:WORD_1
	v_cvt_f32_f16_e32 v126, v58
	s_waitcnt vmcnt(1)
	v_cvt_f32_f16_sdwa v129, v66 dst_sel:DWORD dst_unused:UNUSED_PAD src0_sel:WORD_1
	v_cvt_f32_f16_e32 v128, v66
	v_cvt_f32_f16_sdwa v135, v59 dst_sel:DWORD dst_unused:UNUSED_PAD src0_sel:WORD_1
	v_cvt_f32_f16_e32 v134, v59
	v_cvt_f32_f16_sdwa v137, v67 dst_sel:DWORD dst_unused:UNUSED_PAD src0_sel:WORD_1
	v_cvt_f32_f16_e32 v136, v67
	v_cvt_f32_f16_sdwa v139, v60 dst_sel:DWORD dst_unused:UNUSED_PAD src0_sel:WORD_1
	v_cvt_f32_f16_e32 v138, v60
	v_cvt_f32_f16_sdwa v141, v68 dst_sel:DWORD dst_unused:UNUSED_PAD src0_sel:WORD_1
	v_cvt_f32_f16_e32 v140, v68
	v_cvt_f32_f16_sdwa v143, v61 dst_sel:DWORD dst_unused:UNUSED_PAD src0_sel:WORD_1
	v_cvt_f32_f16_e32 v142, v61
	v_cvt_f32_f16_sdwa v145, v69 dst_sel:DWORD dst_unused:UNUSED_PAD src0_sel:WORD_1
	v_cvt_f32_f16_e32 v144, v69
	v_pk_add_f32 v[126:127], v[128:129], v[126:127]
	v_pk_add_f32 v[128:129], v[136:137], v[134:135]
	v_pk_add_f32 v[134:135], v[140:141], v[138:139]
	v_pk_add_f32 v[136:137], v[144:145], v[142:143]
	v_pk_add_f32 v[106:107], v[106:107], v[126:127]
	v_pk_add_f32 v[110:111], v[110:111], v[128:129]
	v_pk_add_f32 v[108:109], v[108:109], v[134:135]
	v_pk_add_f32 v[112:113], v[112:113], v[136:137]
; __device__ __forceinline__ unsigned pk2h(float lo, float hi) { f32x2 v = {lo, hi}; f16x2 h = __builtin_convertvector(v, f16x2); return __builtin_bit_cast(unsigned, h); }
;     __device__ __forceinline__ void operator()(const f32x4 (&acc)[2][2][4][2], const Unit& u, int wr, int wc, int fr, int fq) const {
;     ...
;                 for (int bj = 0; bj < 2; ++bj) {
;                     f32x4 a0 = acc[ai][bj][m][0], a1 = acc[ai][bj][m][1];
;                     if constexpr (I8) { const i32x4 i0 = __builtin_bit_cast(i32x4, a0), i1 = __builtin_bit_cast(i32x4, a1);
;                         a0 = (f32x4){(float)i0.x, (float)i0.y, (float)i0.z, (float)i0.w} * sv[bj][0]; a1 = (f32x4){(float)i1.x, (float)i1.y, (float)i1.z, (float)i1.w} * sv[bj][1]; }
;                     const f32x4 g0 = a0 * rs[ai][m] + bv[bj][0], g1 = a1 * rs[ai][m] + bv[bj][1];
;                     const f16x8 yy = yv[m][bj];
;                     float z[8];
; #pragma unroll
;                     for (int e = 0; e < 4; ++e) { z[e] = (float)yy[e] * __builtin_amdgcn_rcpf(1.f + __builtin_amdgcn_exp2f(-LOG2E * g0[e])); z[4 + e] = (float)yy[4 + e] * __builtin_amdgcn_rcpf(1.f + __builtin_amdgcn_exp2f(-LOG2E * g1[e])); }
;                     if (br == 2) {
; #pragma unroll
;                         for (int e = 0; e < 8; ++e) z[e] += (float)za[bj][e] + (float)zb[bj][e]; }
;                     u32x4 w; w.x = pk2h(z[0], z[1]); w.y = pk2h(z[2], z[3]); w.z = pk2h(z[4], z[5]); w.w = pk2h(z[6], z[7]);
;                     f16* dst = (br == 2) ? merged : Yb;
;                     gst16(dst + off + bj * HALF, w); } } } }
.LBB0_1267:
	v_cvt_pk_f16_f32 v128, v108, v109
	v_cvt_f32_i32_e32 v108, v104
	v_cvt_f32_i32_e32 v104, v98
	v_cvt_pk_f16_f32 v127, v110, v111
	v_cvt_f32_i32_e32 v110, v99
	v_cvt_f32_i32_e32 v102, v102
	v_mul_f32_e32 v99, v30, v104
	v_fma_f32 v99, v214, v99, v26
	v_exp_f32_e32 v99, v99
	v_cvt_f32_i32_e32 v103, v103
	v_mul_f32_e32 v98, v38, v102
	v_fma_f32 v98, v214, v98, v34
	v_add_f32_e32 v99, 1.0, v99
	v_rcp_f32_e32 v102, v99
	v_mul_f32_e32 v99, v39, v103
	v_fma_f32 v99, v214, v99, v35
	v_exp_f32_e32 v98, v98
	v_exp_f32_e32 v99, v99
	v_mul_f32_e32 v103, v31, v110
	v_fma_f32 v103, v214, v103, v27
	v_pk_add_f32 v[98:99], v[98:99], 1.0 op_sel_hi:[1,0]
	v_exp_f32_e32 v103, v103
	v_cvt_f32_i32_e32 v109, v105
	v_rcp_f32_e32 v98, v98
	v_rcp_f32_e32 v99, v99
	s_waitcnt vmcnt(2)
	v_cvt_f32_f16_sdwa v105, v122 dst_sel:DWORD dst_unused:UNUSED_PAD src0_sel:WORD_1
	v_cvt_f32_f16_e32 v104, v122
	v_add_f32_e32 v103, 1.0, v103
	v_rcp_f32_e32 v103, v103
	v_cvt_pk_f16_f32 v126, v106, v107
	v_pk_mul_f32 v[98:99], v[98:99], v[104:105]
	v_cvt_f32_f16_sdwa v105, v124 dst_sel:DWORD dst_unused:UNUSED_PAD src0_sel:WORD_1
	v_cvt_f32_f16_e32 v104, v124
	v_cvt_pk_f16_f32 v129, v112, v113
	v_lshl_add_u64 v[106:107], v[130:131], 1, s[46:47]
	s_mov_b64 s[46:47], -1
	v_pk_mul_f32 v[102:103], v[102:103], v[104:105]
	v_mul_f32_e32 v104, v40, v108
	v_mul_f32_e32 v105, v41, v109
	v_fma_f32 v104, v214, v104, v36
	v_fma_f32 v105, v214, v105, v37
	v_exp_f32_e32 v104, v104
	v_exp_f32_e32 v105, v105
	v_cvt_f32_f16_sdwa v109, v123 dst_sel:DWORD dst_unused:UNUSED_PAD src0_sel:WORD_1
	v_cvt_f32_f16_e32 v108, v123
	v_pk_add_f32 v[104:105], v[104:105], 1.0 op_sel_hi:[1,0]
	v_rcp_f32_e32 v104, v104
	v_rcp_f32_e32 v105, v105
	s_and_b64 vcc, exec, s[38:39]
	s_mov_b64 s[28:29], 0x2000
	v_lshl_add_u64 v[222:223], v[224:225], 0, s[28:29]
	v_cndmask_b32_e64 v222, v106, v222, s[36:37]
	v_cndmask_b32_e64 v223, v107, v223, s[36:37]
	global_store_dwordx4 v[222:223], v[126:129], off
	v_pk_mul_f32 v[104:105], v[104:105], v[108:109]
	s_cbranch_vccnz .LBB0_1269
	s_mov_b64 s[46:47], 0
.LBB0_1269:
	v_cvt_f32_i32_e32 v100, v100
	v_cvt_f32_i32_e32 v101, v101
	v_cvt_f32_f16_sdwa v109, v125 dst_sel:DWORD dst_unused:UNUSED_PAD src0_sel:WORD_1
	v_cvt_f32_f16_e32 v108, v125
	v_mul_f32_e32 v100, v32, v100
	v_mul_f32_e32 v101, v33, v101
	v_fma_f32 v100, v214, v100, v28
	v_fma_f32 v101, v214, v101, v29
	v_exp_f32_e32 v100, v100
	v_exp_f32_e32 v101, v101
	s_andn2_b64 vcc, exec, s[46:47]
	v_pk_add_f32 v[100:101], v[100:101], 1.0 op_sel_hi:[1,0]
	v_rcp_f32_e32 v100, v100
	v_rcp_f32_e32 v101, v101
	s_nop 0
	v_pk_mul_f32 v[100:101], v[100:101], v[108:109]
	s_cbranch_vccnz .LBB0_1271
	v_cvt_f32_f16_sdwa v109, v42 dst_sel:DWORD dst_unused:UNUSED_PAD src0_sel:WORD_1
	v_cvt_f32_f16_e32 v108, v42
	s_waitcnt vmcnt(1)
	v_cvt_f32_f16_sdwa v111, v46 dst_sel:DWORD dst_unused:UNUSED_PAD src0_sel:WORD_1
	v_cvt_f32_f16_e32 v110, v46
	v_cvt_f32_f16_sdwa v113, v43 dst_sel:DWORD dst_unused:UNUSED_PAD src0_sel:WORD_1
	v_cvt_f32_f16_e32 v112, v43
	v_cvt_f32_f16_sdwa v123, v47 dst_sel:DWORD dst_unused:UNUSED_PAD src0_sel:WORD_1
	v_cvt_f32_f16_e32 v122, v47
	v_cvt_f32_f16_sdwa v125, v44 dst_sel:DWORD dst_unused:UNUSED_PAD src0_sel:WORD_1
	v_cvt_f32_f16_e32 v124, v44
	v_cvt_f32_f16_sdwa v127, v48 dst_sel:DWORD dst_unused:UNUSED_PAD src0_sel:WORD_1
	v_cvt_f32_f16_e32 v126, v48
	v_cvt_f32_f16_sdwa v129, v45 dst_sel:DWORD dst_unused:UNUSED_PAD src0_sel:WORD_1
	v_cvt_f32_f16_e32 v128, v45
	v_cvt_f32_f16_sdwa v135, v49 dst_sel:DWORD dst_unused:UNUSED_PAD src0_sel:WORD_1
	v_cvt_f32_f16_e32 v134, v49
	v_pk_add_f32 v[108:109], v[110:111], v[108:109]
	v_pk_add_f32 v[110:111], v[122:123], v[112:113]
	v_pk_add_f32 v[112:113], v[126:127], v[124:125]
	v_pk_add_f32 v[122:123], v[134:135], v[128:129]
	v_pk_add_f32 v[98:99], v[98:99], v[108:109]
	v_pk_add_f32 v[104:105], v[104:105], v[110:111]
	v_pk_add_f32 v[102:103], v[102:103], v[112:113]
	v_pk_add_f32 v[100:101], v[100:101], v[122:123]

;     __device__ __forceinline__ void operator()(const f32x4 (&acc)[2][2][4][2], const Unit& u, int wr, int wc, int fr, int fq) const {
;     ...
;                 for (int bj = 0; bj < 2; ++bj) {
;                     f32x4 a0 = acc[ai][bj][m][0], a1 = acc[ai][bj][m][1];
;                     if constexpr (I8) { const i32x4 i0 = __builtin_bit_cast(i32x4, a0), i1 = __builtin_bit_cast(i32x4, a1);
;                         a0 = (f32x4){(float)i0.x, (float)i0.y, (float)i0.z, (float)i0.w} * sv[bj][0]; a1 = (f32x4){(float)i1.x, (float)i1.y, (float)i1.z, (float)i1.w} * sv[bj][1]; }
;                     const f32x4 g0 = a0 * rs[ai][m] + bv[bj][0], g1 = a1 * rs[ai][m] + bv[bj][1];
;                     const f16x8 yy = yv[m][bj];
;                     float z[8];
; #pragma unroll
;                     for (int e = 0; e < 4; ++e) { z[e] = (float)yy[e] * __builtin_amdgcn_rcpf(1.f + __builtin_amdgcn_exp2f(-LOG2E * g0[e])); z[4 + e] = (float)yy[4 + e] * __builtin_amdgcn_rcpf(1.f + __builtin_amdgcn_exp2f(-LOG2E * g1[e])); }
;                     if (br == 2) {
; #pragma unroll
;                         for (int e = 0; e < 8; ++e) z[e] += (float)za[bj][e] + (float)zb[bj][e]; }
.LBB0_1273:
	v_cvt_f32_i32_e32 v98, v90
	v_cvt_f32_i32_e32 v99, v91
	v_cvt_f32_i32_e32 v94, v94
	v_cvt_f32_i32_e32 v95, v95
	v_mul_f32_e32 v91, v54, v98
	v_fma_f32 v91, v215, v91, v50
	v_exp_f32_e32 v91, v91
	v_cvt_f32_i32_e32 v100, v92
	v_mul_f32_e32 v90, v70, v94
	v_fma_f32 v90, v215, v90, v62
	v_add_f32_e32 v91, 1.0, v91
	v_rcp_f32_e32 v92, v91
	v_mul_f32_e32 v91, v71, v95
	v_fma_f32 v91, v215, v91, v63
	v_exp_f32_e32 v90, v90
	v_exp_f32_e32 v91, v91
	v_cvt_f32_i32_e32 v101, v93
	v_mul_f32_e32 v93, v55, v99
	v_fma_f32 v93, v215, v93, v51
	v_pk_add_f32 v[90:91], v[90:91], 1.0 op_sel_hi:[1,0]
	v_exp_f32_e32 v93, v93
	v_rcp_f32_e32 v90, v90
	v_rcp_f32_e32 v91, v91
	s_waitcnt vmcnt(3)
	v_cvt_f32_f16_sdwa v95, v118 dst_sel:DWORD dst_unused:UNUSED_PAD src0_sel:WORD_1
	v_cvt_f32_f16_e32 v94, v118
	v_add_f32_e32 v93, 1.0, v93
	v_rcp_f32_e32 v93, v93
	v_cvt_f32_i32_e32 v96, v96
	v_pk_mul_f32 v[90:91], v[90:91], v[94:95]
	v_cvt_f32_f16_sdwa v95, v120 dst_sel:DWORD dst_unused:UNUSED_PAD src0_sel:WORD_1
	v_cvt_f32_f16_e32 v94, v120
	v_cvt_f32_i32_e32 v97, v97
	v_cvt_f32_f16_sdwa v99, v119 dst_sel:DWORD dst_unused:UNUSED_PAD src0_sel:WORD_1
	v_cvt_f32_f16_e32 v98, v119
	v_pk_mul_f32 v[92:93], v[92:93], v[94:95]
	v_mul_f32_e32 v95, v56, v100
	v_fma_f32 v95, v215, v95, v52
	v_exp_f32_e32 v95, v95
	v_mul_f32_e32 v94, v72, v96
	v_fma_f32 v94, v215, v94, v64
	v_add_f32_e32 v95, 1.0, v95
	v_rcp_f32_e32 v96, v95
	v_mul_f32_e32 v95, v73, v97
	v_fma_f32 v95, v215, v95, v65
	v_exp_f32_e32 v94, v94
	v_exp_f32_e32 v95, v95
	v_mul_f32_e32 v97, v57, v101
	v_fma_f32 v97, v215, v97, v53
	v_pk_add_f32 v[94:95], v[94:95], 1.0 op_sel_hi:[1,0]
	v_exp_f32_e32 v97, v97
	v_rcp_f32_e32 v94, v94
	v_rcp_f32_e32 v95, v95
	s_and_b64 vcc, exec, s[36:37]
	v_add_f32_e32 v97, 1.0, v97
	v_rcp_f32_e32 v97, v97
	v_pk_mul_f32 v[94:95], v[94:95], v[98:99]
	v_cvt_f32_f16_sdwa v99, v121 dst_sel:DWORD dst_unused:UNUSED_PAD src0_sel:WORD_1
	v_cvt_f32_f16_e32 v98, v121
	v_pk_mul_f32 v[96:97], v[96:97], v[98:99]
	s_cbranch_vccnz .LBB0_1275
	v_cvt_f32_f16_sdwa v99, v58 dst_sel:DWORD dst_unused:UNUSED_PAD src0_sel:WORD_1
	v_cvt_f32_f16_e32 v98, v58
	s_waitcnt vmcnt(1)
	v_cvt_f32_f16_sdwa v101, v66 dst_sel:DWORD dst_unused:UNUSED_PAD src0_sel:WORD_1
	v_cvt_f32_f16_e32 v100, v66
	v_cvt_f32_f16_sdwa v103, v59 dst_sel:DWORD dst_unused:UNUSED_PAD src0_sel:WORD_1
	v_cvt_f32_f16_e32 v102, v59
	v_cvt_f32_f16_sdwa v105, v67 dst_sel:DWORD dst_unused:UNUSED_PAD src0_sel:WORD_1
	v_cvt_f32_f16_e32 v104, v67
	v_cvt_f32_f16_sdwa v109, v60 dst_sel:DWORD dst_unused:UNUSED_PAD src0_sel:WORD_1
	v_cvt_f32_f16_e32 v108, v60
	v_cvt_f32_f16_sdwa v111, v68 dst_sel:DWORD dst_unused:UNUSED_PAD src0_sel:WORD_1
	v_cvt_f32_f16_e32 v110, v68
	v_cvt_f32_f16_sdwa v113, v61 dst_sel:DWORD dst_unused:UNUSED_PAD src0_sel:WORD_1
	v_cvt_f32_f16_e32 v112, v61
	v_cvt_f32_f16_sdwa v119, v69 dst_sel:DWORD dst_unused:UNUSED_PAD src0_sel:WORD_1
	v_cvt_f32_f16_e32 v118, v69
	v_pk_add_f32 v[98:99], v[100:101], v[98:99]
	v_pk_add_f32 v[100:101], v[104:105], v[102:103]
	v_pk_add_f32 v[102:103], v[110:111], v[108:109]
	v_pk_add_f32 v[104:105], v[118:119], v[112:113]
	v_pk_add_f32 v[90:91], v[90:91], v[98:99]
	v_pk_add_f32 v[94:95], v[94:95], v[100:101]
	v_pk_add_f32 v[92:93], v[92:93], v[102:103]
	v_pk_add_f32 v[96:97], v[96:97], v[104:105]
; __device__ __forceinline__ unsigned pk2h(float lo, float hi) { f32x2 v = {lo, hi}; f16x2 h = __builtin_convertvector(v, f16x2); return __builtin_bit_cast(unsigned, h); }
;     __device__ __forceinline__ void operator()(const f32x4 (&acc)[2][2][4][2], const Unit& u, int wr, int wc, int fr, int fq) const {
;     ...
;                 for (int bj = 0; bj < 2; ++bj) {
;                     f32x4 a0 = acc[ai][bj][m][0], a1 = acc[ai][bj][m][1];
;                     if constexpr (I8) { const i32x4 i0 = __builtin_bit_cast(i32x4, a0), i1 = __builtin_bit_cast(i32x4, a1);
;                         a0 = (f32x4){(float)i0.x, (float)i0.y, (float)i0.z, (float)i0.w} * sv[bj][0]; a1 = (f32x4){(float)i1.x, (float)i1.y, (float)i1.z, (float)i1.w} * sv[bj][1]; }
;                     const f32x4 g0 = a0 * rs[ai][m] + bv[bj][0], g1 = a1 * rs[ai][m] + bv[bj][1];
;                     const f16x8 yy = yv[m][bj];
;                     float z[8];
; #pragma unroll
;                     for (int e = 0; e < 4; ++e) { z[e] = (float)yy[e] * __builtin_amdgcn_rcpf(1.f + __builtin_amdgcn_exp2f(-LOG2E * g0[e])); z[4 + e] = (float)yy[4 + e] * __builtin_amdgcn_rcpf(1.f + __builtin_amdgcn_exp2f(-LOG2E * g1[e])); }
;                     if (br == 2) {
; #pragma unroll
;                         for (int e = 0; e < 8; ++e) z[e] += (float)za[bj][e] + (float)zb[bj][e]; }
;                     u32x4 w; w.x = pk2h(z[0], z[1]); w.y = pk2h(z[2], z[3]); w.z = pk2h(z[4], z[5]); w.w = pk2h(z[6], z[7]);
;                     f16* dst = (br == 2) ? merged : Yb;
;                     gst16(dst + off + bj * HALF, w); } } } }
.LBB0_1275:
	s_mov_b32 s26, 0x8000
	v_cvt_pk_f16_f32 v90, v90, v91
	v_cvt_pk_f16_f32 v91, v94, v95
	v_add_co_u32_e32 v94, vcc, s26, v106
	v_cvt_pk_f16_f32 v92, v92, v93
	v_cvt_pk_f16_f32 v93, v96, v97
	v_addc_co_u32_e32 v95, vcc, 0, v107, vcc
	s_mov_b64 s[28:29], 0x2800
	v_lshl_add_u64 v[222:223], v[224:225], 0, s[28:29]
	v_cndmask_b32_e64 v222, v94, v222, s[36:37]
	v_cndmask_b32_e64 v223, v95, v223, s[36:37]
	global_store_dwordx4 v[222:223], v[90:93], off
	v_cvt_f32_i32_e32 v86, v86
	v_cvt_f32_i32_e32 v87, v87
	v_cvt_f32_i32_e32 v90, v88
	v_cvt_f32_i32_e32 v88, v82
	v_cvt_f32_i32_e32 v92, v83
	v_mul_f32_e32 v82, v38, v86
	v_fma_f32 v82, v215, v82, v34
	v_mul_f32_e32 v83, v30, v88
	v_fma_f32 v83, v215, v83, v26
	v_exp_f32_e32 v83, v83
	v_exp_f32_e32 v82, v82
	v_cvt_f32_i32_e32 v91, v89
	v_add_f32_e32 v83, 1.0, v83
	v_rcp_f32_e32 v86, v83
	v_mul_f32_e32 v83, v39, v87
	v_fma_f32 v83, v215, v83, v35
	v_exp_f32_e32 v83, v83
	v_mul_f32_e32 v87, v31, v92
	v_fma_f32 v87, v215, v87, v27
	v_pk_add_f32 v[82:83], v[82:83], 1.0 op_sel_hi:[1,0]
	v_exp_f32_e32 v87, v87
	v_rcp_f32_e32 v82, v82
	v_rcp_f32_e32 v83, v83
	s_waitcnt vmcnt(3)
	v_cvt_f32_f16_sdwa v89, v114 dst_sel:DWORD dst_unused:UNUSED_PAD src0_sel:WORD_1
	v_cvt_f32_f16_e32 v88, v114
	v_add_f32_e32 v87, 1.0, v87
	v_rcp_f32_e32 v87, v87
	s_mov_b64 s[46:47], -1
	v_pk_mul_f32 v[82:83], v[82:83], v[88:89]
	v_cvt_f32_f16_sdwa v89, v116 dst_sel:DWORD dst_unused:UNUSED_PAD src0_sel:WORD_1
	v_cvt_f32_f16_e32 v88, v116
	s_and_b64 vcc, exec, s[38:39]
	v_pk_mul_f32 v[86:87], v[86:87], v[88:89]
	v_mul_f32_e32 v88, v40, v90
	v_mul_f32_e32 v89, v41, v91
	v_fma_f32 v88, v215, v88, v36
	v_fma_f32 v89, v215, v89, v37
	v_exp_f32_e32 v88, v88
	v_exp_f32_e32 v89, v89
	v_cvt_f32_f16_sdwa v91, v115 dst_sel:DWORD dst_unused:UNUSED_PAD src0_sel:WORD_1
	v_cvt_f32_f16_e32 v90, v115
	v_pk_add_f32 v[88:89], v[88:89], 1.0 op_sel_hi:[1,0]
	v_rcp_f32_e32 v88, v88
	v_rcp_f32_e32 v89, v89
	s_nop 0
	v_pk_mul_f32 v[88:89], v[88:89], v[90:91]
	s_cbranch_vccnz .LBB0_1277
	s_mov_b64 s[46:47], 0
.LBB0_1277:
	v_cvt_f32_i32_e32 v84, v84
	v_cvt_f32_i32_e32 v85, v85
	v_cvt_f32_f16_sdwa v91, v117 dst_sel:DWORD dst_unused:UNUSED_PAD src0_sel:WORD_1
	v_cvt_f32_f16_e32 v90, v117
	v_mul_f32_e32 v84, v32, v84
	v_mul_f32_e32 v85, v33, v85
	v_fma_f32 v84, v215, v84, v28
	v_fma_f32 v85, v215, v85, v29
	v_exp_f32_e32 v84, v84
	v_exp_f32_e32 v85, v85
	s_andn2_b64 vcc, exec, s[46:47]
	v_pk_add_f32 v[84:85], v[84:85], 1.0 op_sel_hi:[1,0]
	v_rcp_f32_e32 v84, v84
	v_rcp_f32_e32 v85, v85
	s_nop 0
	v_pk_mul_f32 v[84:85], v[84:85], v[90:91]
	s_cbranch_vccnz .LBB0_1279
	v_cvt_f32_f16_sdwa v91, v42 dst_sel:DWORD dst_unused:UNUSED_PAD src0_sel:WORD_1
	v_cvt_f32_f16_e32 v90, v42
	s_waitcnt vmcnt(1)
	v_cvt_f32_f16_sdwa v93, v46 dst_sel:DWORD dst_unused:UNUSED_PAD src0_sel:WORD_1
	v_cvt_f32_f16_e32 v92, v46
	v_cvt_f32_f16_sdwa v95, v43 dst_sel:DWORD dst_unused:UNUSED_PAD src0_sel:WORD_1
	v_cvt_f32_f16_e32 v94, v43
	v_cvt_f32_f16_sdwa v97, v47 dst_sel:DWORD dst_unused:UNUSED_PAD src0_sel:WORD_1
	v_cvt_f32_f16_e32 v96, v47
	v_cvt_f32_f16_sdwa v99, v44 dst_sel:DWORD dst_unused:UNUSED_PAD src0_sel:WORD_1
	v_cvt_f32_f16_e32 v98, v44
	v_cvt_f32_f16_sdwa v101, v48 dst_sel:DWORD dst_unused:UNUSED_PAD src0_sel:WORD_1
	v_cvt_f32_f16_e32 v100, v48
	v_cvt_f32_f16_sdwa v103, v45 dst_sel:DWORD dst_unused:UNUSED_PAD src0_sel:WORD_1
	v_cvt_f32_f16_e32 v102, v45
	v_cvt_f32_f16_sdwa v105, v49 dst_sel:DWORD dst_unused:UNUSED_PAD src0_sel:WORD_1
	v_cvt_f32_f16_e32 v104, v49
	v_pk_add_f32 v[90:91], v[92:93], v[90:91]
	v_pk_add_f32 v[92:93], v[96:97], v[94:95]
	v_pk_add_f32 v[94:95], v[100:101], v[98:99]
	v_pk_add_f32 v[96:97], v[104:105], v[102:103]
	v_pk_add_f32 v[82:83], v[82:83], v[90:91]
	v_pk_add_f32 v[88:89], v[88:89], v[92:93]
	v_pk_add_f32 v[86:87], v[86:87], v[94:95]
	v_pk_add_f32 v[84:85], v[84:85], v[96:97]

;     __device__ __forceinline__ void operator()(const f32x4 (&acc)[2][2][4][2], const Unit& u, int wr, int wc, int fr, int fq) const {
;     ...
;                 for (int bj = 0; bj < 2; ++bj) {
;                     f32x4 a0 = acc[ai][bj][m][0], a1 = acc[ai][bj][m][1];
;                     if constexpr (I8) { const i32x4 i0 = __builtin_bit_cast(i32x4, a0), i1 = __builtin_bit_cast(i32x4, a1);
;                         a0 = (f32x4){(float)i0.x, (float)i0.y, (float)i0.z, (float)i0.w} * sv[bj][0]; a1 = (f32x4){(float)i1.x, (float)i1.y, (float)i1.z, (float)i1.w} * sv[bj][1]; }
;                     const f32x4 g0 = a0 * rs[ai][m] + bv[bj][0], g1 = a1 * rs[ai][m] + bv[bj][1];
;                     const f16x8 yy = yv[m][bj];
;                     float z[8];
; #pragma unroll
;                     for (int e = 0; e < 4; ++e) { z[e] = (float)yy[e] * __builtin_amdgcn_rcpf(1.f + __builtin_amdgcn_exp2f(-LOG2E * g0[e])); z[4 + e] = (float)yy[4 + e] * __builtin_amdgcn_rcpf(1.f + __builtin_amdgcn_exp2f(-LOG2E * g1[e])); }
;                     if (br == 2) {
; #pragma unroll
;                         for (int e = 0; e < 8; ++e) z[e] += (float)za[bj][e] + (float)zb[bj][e]; }
.LBB0_1281:
	v_cvt_f32_i32_e32 v98, v74
	v_cvt_f32_i32_e32 v99, v75
	v_cvt_f32_i32_e32 v78, v78
	v_cvt_f32_i32_e32 v79, v79
	v_mul_f32_e32 v75, v54, v98
	v_fma_f32 v75, v212, v75, v50
	v_exp_f32_e32 v75, v75
	v_cvt_f32_i32_e32 v100, v76
	v_mul_f32_e32 v74, v70, v78
	v_fma_f32 v74, v212, v74, v62
	v_add_f32_e32 v75, 1.0, v75
	v_rcp_f32_e32 v76, v75
	v_mul_f32_e32 v75, v71, v79
	v_fma_f32 v75, v212, v75, v63
	v_exp_f32_e32 v74, v74
	v_exp_f32_e32 v75, v75
	v_cvt_f32_i32_e32 v101, v77
	v_mul_f32_e32 v77, v55, v99
	v_fma_f32 v77, v212, v77, v51
	v_pk_add_f32 v[74:75], v[74:75], 1.0 op_sel_hi:[1,0]
	v_exp_f32_e32 v77, v77
	v_rcp_f32_e32 v74, v74
	v_rcp_f32_e32 v75, v75
	s_waitcnt vmcnt(3)
	v_cvt_f32_f16_sdwa v79, v94 dst_sel:DWORD dst_unused:UNUSED_PAD src0_sel:WORD_1
	v_cvt_f32_f16_e32 v78, v94
	v_add_f32_e32 v77, 1.0, v77
	v_rcp_f32_e32 v77, v77
	v_cvt_f32_i32_e32 v80, v80
	v_pk_mul_f32 v[74:75], v[74:75], v[78:79]
	v_cvt_f32_f16_sdwa v79, v96 dst_sel:DWORD dst_unused:UNUSED_PAD src0_sel:WORD_1
	v_cvt_f32_f16_e32 v78, v96
	v_cvt_f32_i32_e32 v81, v81
	v_cvt_f32_f16_sdwa v99, v95 dst_sel:DWORD dst_unused:UNUSED_PAD src0_sel:WORD_1
	v_cvt_f32_f16_e32 v98, v95
	v_pk_mul_f32 v[76:77], v[76:77], v[78:79]
	v_mul_f32_e32 v79, v56, v100
	v_fma_f32 v79, v212, v79, v52
	v_exp_f32_e32 v79, v79
	v_mul_f32_e32 v78, v72, v80
	v_fma_f32 v78, v212, v78, v64
	v_add_f32_e32 v79, 1.0, v79
	v_rcp_f32_e32 v80, v79
	v_mul_f32_e32 v79, v73, v81
	v_mul_f32_e32 v81, v57, v101
	v_fma_f32 v79, v212, v79, v65
	v_fma_f32 v81, v212, v81, v53
	v_exp_f32_e32 v78, v78
	v_exp_f32_e32 v79, v79
	v_exp_f32_e32 v81, v81
	v_cvt_f32_f16_sdwa v95, v97 dst_sel:DWORD dst_unused:UNUSED_PAD src0_sel:WORD_1
	v_pk_add_f32 v[78:79], v[78:79], 1.0 op_sel_hi:[1,0]
	v_add_f32_e32 v81, 1.0, v81
	v_rcp_f32_e32 v78, v78
	v_rcp_f32_e32 v79, v79
	v_rcp_f32_e32 v81, v81
	v_cvt_f32_f16_e32 v94, v97
	s_and_b64 vcc, exec, s[36:37]
	v_pk_mul_f32 v[78:79], v[78:79], v[98:99]
	v_pk_mul_f32 v[80:81], v[80:81], v[94:95]
	s_cbranch_vccnz .LBB0_1283
	v_cvt_f32_f16_sdwa v95, v58 dst_sel:DWORD dst_unused:UNUSED_PAD src0_sel:WORD_1
	v_cvt_f32_f16_e32 v94, v58
	s_waitcnt vmcnt(1)
	v_cvt_f32_f16_sdwa v97, v66 dst_sel:DWORD dst_unused:UNUSED_PAD src0_sel:WORD_1
	v_cvt_f32_f16_e32 v96, v66
	v_cvt_f32_f16_sdwa v99, v59 dst_sel:DWORD dst_unused:UNUSED_PAD src0_sel:WORD_1
	v_cvt_f32_f16_e32 v98, v59
	v_cvt_f32_f16_sdwa v101, v67 dst_sel:DWORD dst_unused:UNUSED_PAD src0_sel:WORD_1
	v_cvt_f32_f16_e32 v100, v67
	v_cvt_f32_f16_sdwa v103, v60 dst_sel:DWORD dst_unused:UNUSED_PAD src0_sel:WORD_1
	v_cvt_f32_f16_e32 v102, v60
	v_cvt_f32_f16_sdwa v105, v68 dst_sel:DWORD dst_unused:UNUSED_PAD src0_sel:WORD_1
	v_cvt_f32_f16_e32 v104, v68
	v_cvt_f32_f16_sdwa v109, v61 dst_sel:DWORD dst_unused:UNUSED_PAD src0_sel:WORD_1
	v_cvt_f32_f16_e32 v108, v61
	v_cvt_f32_f16_sdwa v111, v69 dst_sel:DWORD dst_unused:UNUSED_PAD src0_sel:WORD_1
	v_cvt_f32_f16_e32 v110, v69
	v_pk_add_f32 v[94:95], v[96:97], v[94:95]
	v_pk_add_f32 v[96:97], v[100:101], v[98:99]
	v_pk_add_f32 v[98:99], v[104:105], v[102:103]
	v_pk_add_f32 v[100:101], v[110:111], v[108:109]
	v_pk_add_f32 v[74:75], v[74:75], v[94:95]
	v_pk_add_f32 v[78:79], v[78:79], v[96:97]
	v_pk_add_f32 v[76:77], v[76:77], v[98:99]
	v_pk_add_f32 v[80:81], v[80:81], v[100:101]
; __device__ __forceinline__ unsigned pk2h(float lo, float hi) { f32x2 v = {lo, hi}; f16x2 h = __builtin_convertvector(v, f16x2); return __builtin_bit_cast(unsigned, h); }
;     __device__ __forceinline__ void operator()(const f32x4 (&acc)[2][2][4][2], const Unit& u, int wr, int wc, int fr, int fq) const {
;     ...
;                 for (int bj = 0; bj < 2; ++bj) {
;                     f32x4 a0 = acc[ai][bj][m][0], a1 = acc[ai][bj][m][1];
;                     if constexpr (I8) { const i32x4 i0 = __builtin_bit_cast(i32x4, a0), i1 = __builtin_bit_cast(i32x4, a1);
;                         a0 = (f32x4){(float)i0.x, (float)i0.y, (float)i0.z, (float)i0.w} * sv[bj][0]; a1 = (f32x4){(float)i1.x, (float)i1.y, (float)i1.z, (float)i1.w} * sv[bj][1]; }
;                     const f32x4 g0 = a0 * rs[ai][m] + bv[bj][0], g1 = a1 * rs[ai][m] + bv[bj][1];
;                     const f16x8 yy = yv[m][bj];
;                     float z[8];
; #pragma unroll
;                     for (int e = 0; e < 4; ++e) { z[e] = (float)yy[e] * __builtin_amdgcn_rcpf(1.f + __builtin_amdgcn_exp2f(-LOG2E * g0[e])); z[4 + e] = (float)yy[4 + e] * __builtin_amdgcn_rcpf(1.f + __builtin_amdgcn_exp2f(-LOG2E * g1[e])); }
;                     if (br == 2) {
; #pragma unroll
;                         for (int e = 0; e < 8; ++e) z[e] += (float)za[bj][e] + (float)zb[bj][e]; }
;                     u32x4 w; w.x = pk2h(z[0], z[1]); w.y = pk2h(z[2], z[3]); w.z = pk2h(z[4], z[5]); w.w = pk2h(z[6], z[7]);
;                     f16* dst = (br == 2) ? merged : Yb;
;                     gst16(dst + off + bj * HALF, w); } } } }
.LBB0_1283:
	s_mov_b32 s26, 0x10000
	v_cvt_pk_f16_f32 v74, v74, v75
	v_cvt_pk_f16_f32 v75, v78, v79
	v_add_co_u32_e32 v78, vcc, s26, v106
	v_cvt_pk_f16_f32 v76, v76, v77
	v_cvt_pk_f16_f32 v77, v80, v81
	v_addc_co_u32_e32 v79, vcc, 0, v107, vcc
	s_mov_b64 s[28:29], 0x3000
	v_lshl_add_u64 v[222:223], v[224:225], 0, s[28:29]
	v_cndmask_b32_e64 v222, v78, v222, s[36:37]
	v_cndmask_b32_e64 v223, v79, v223, s[36:37]
	global_store_dwordx4 v[222:223], v[74:77], off
	v_cvt_f32_i32_e32 v22, v22
	v_cvt_f32_i32_e32 v23, v23
	v_cvt_f32_i32_e32 v74, v24
	v_cvt_f32_i32_e32 v24, v18
	v_cvt_f32_i32_e32 v76, v19
	v_mul_f32_e32 v18, v38, v22
	v_fma_f32 v18, v212, v18, v34
	v_mul_f32_e32 v19, v30, v24
	v_fma_f32 v19, v212, v19, v26
	v_exp_f32_e32 v19, v19
	v_exp_f32_e32 v18, v18
	v_cvt_f32_i32_e32 v75, v25
	v_add_f32_e32 v19, 1.0, v19
	v_rcp_f32_e32 v22, v19
	v_mul_f32_e32 v19, v39, v23
	v_fma_f32 v19, v212, v19, v35
	v_exp_f32_e32 v19, v19
	v_mul_f32_e32 v23, v31, v76
	v_fma_f32 v23, v212, v23, v27
	v_pk_add_f32 v[18:19], v[18:19], 1.0 op_sel_hi:[1,0]
	v_exp_f32_e32 v23, v23
	v_rcp_f32_e32 v18, v18
	v_rcp_f32_e32 v19, v19
	s_waitcnt vmcnt(3)
	v_cvt_f32_f16_sdwa v25, v90 dst_sel:DWORD dst_unused:UNUSED_PAD src0_sel:WORD_1
	v_cvt_f32_f16_e32 v24, v90
	v_add_f32_e32 v23, 1.0, v23
	v_rcp_f32_e32 v23, v23
	s_mov_b64 s[46:47], -1
	v_pk_mul_f32 v[18:19], v[18:19], v[24:25]
	v_cvt_f32_f16_sdwa v25, v92 dst_sel:DWORD dst_unused:UNUSED_PAD src0_sel:WORD_1
	v_cvt_f32_f16_e32 v24, v92
	s_and_b64 vcc, exec, s[38:39]
	v_pk_mul_f32 v[22:23], v[22:23], v[24:25]
	v_mul_f32_e32 v24, v40, v74
	v_mul_f32_e32 v25, v41, v75
	v_fma_f32 v24, v212, v24, v36
	v_fma_f32 v25, v212, v25, v37
	v_exp_f32_e32 v24, v24
	v_exp_f32_e32 v25, v25
	v_cvt_f32_f16_sdwa v75, v91 dst_sel:DWORD dst_unused:UNUSED_PAD src0_sel:WORD_1
	v_cvt_f32_f16_e32 v74, v91
	v_pk_add_f32 v[24:25], v[24:25], 1.0 op_sel_hi:[1,0]
	v_rcp_f32_e32 v24, v24
	v_rcp_f32_e32 v25, v25
	s_nop 0
	v_pk_mul_f32 v[24:25], v[24:25], v[74:75]
	s_cbranch_vccnz .LBB0_1285
	s_mov_b64 s[46:47], 0
.LBB0_1285:
	v_cvt_f32_i32_e32 v20, v20
	v_cvt_f32_i32_e32 v21, v21
	v_cvt_f32_f16_sdwa v75, v93 dst_sel:DWORD dst_unused:UNUSED_PAD src0_sel:WORD_1
	v_cvt_f32_f16_e32 v74, v93
	v_mul_f32_e32 v20, v32, v20
	v_mul_f32_e32 v21, v33, v21
	v_fma_f32 v20, v212, v20, v28
	v_fma_f32 v21, v212, v21, v29
	v_exp_f32_e32 v20, v20
	v_exp_f32_e32 v21, v21
	s_andn2_b64 vcc, exec, s[46:47]
	v_pk_add_f32 v[20:21], v[20:21], 1.0 op_sel_hi:[1,0]
	v_rcp_f32_e32 v20, v20
	v_rcp_f32_e32 v21, v21
	s_nop 0
	v_pk_mul_f32 v[20:21], v[20:21], v[74:75]
	s_cbranch_vccnz .LBB0_1287
	v_cvt_f32_f16_sdwa v75, v42 dst_sel:DWORD dst_unused:UNUSED_PAD src0_sel:WORD_1
	v_cvt_f32_f16_e32 v74, v42
	s_waitcnt vmcnt(1)
	v_cvt_f32_f16_sdwa v77, v46 dst_sel:DWORD dst_unused:UNUSED_PAD src0_sel:WORD_1
	v_cvt_f32_f16_e32 v76, v46
	v_cvt_f32_f16_sdwa v79, v43 dst_sel:DWORD dst_unused:UNUSED_PAD src0_sel:WORD_1
	v_cvt_f32_f16_e32 v78, v43
	v_cvt_f32_f16_sdwa v81, v47 dst_sel:DWORD dst_unused:UNUSED_PAD src0_sel:WORD_1
	v_cvt_f32_f16_e32 v80, v47
	v_cvt_f32_f16_sdwa v91, v44 dst_sel:DWORD dst_unused:UNUSED_PAD src0_sel:WORD_1
	v_cvt_f32_f16_e32 v90, v44
	v_cvt_f32_f16_sdwa v93, v48 dst_sel:DWORD dst_unused:UNUSED_PAD src0_sel:WORD_1
	v_cvt_f32_f16_e32 v92, v48
	v_cvt_f32_f16_sdwa v95, v45 dst_sel:DWORD dst_unused:UNUSED_PAD src0_sel:WORD_1
	v_cvt_f32_f16_e32 v94, v45
	v_cvt_f32_f16_sdwa v97, v49 dst_sel:DWORD dst_unused:UNUSED_PAD src0_sel:WORD_1
	v_cvt_f32_f16_e32 v96, v49
	v_pk_add_f32 v[74:75], v[76:77], v[74:75]
	v_pk_add_f32 v[76:77], v[80:81], v[78:79]
	v_pk_add_f32 v[78:79], v[92:93], v[90:91]
	v_pk_add_f32 v[80:81], v[96:97], v[94:95]
	v_pk_add_f32 v[18:19], v[18:19], v[74:75]
	v_pk_add_f32 v[24:25], v[24:25], v[76:77]
	v_pk_add_f32 v[22:23], v[22:23], v[78:79]
	v_pk_add_f32 v[20:21], v[20:21], v[80:81]

; __device__ __forceinline__ unsigned pk2h(float lo, float hi) { f32x2 v = {lo, hi}; f16x2 h = __builtin_convertvector(v, f16x2); return __builtin_bit_cast(unsigned, h); }
;     __device__ __forceinline__ void operator()(const f32x4 (&acc)[2][2][4][2], const Unit& u, int wr, int wc, int fr, int fq) const {
;     ...
;                 for (int bj = 0; bj < 2; ++bj) {
;                     f32x4 a0 = acc[ai][bj][m][0], a1 = acc[ai][bj][m][1];
;                     if constexpr (I8) { const i32x4 i0 = __builtin_bit_cast(i32x4, a0), i1 = __builtin_bit_cast(i32x4, a1);
;                         a0 = (f32x4){(float)i0.x, (float)i0.y, (float)i0.z, (float)i0.w} * sv[bj][0]; a1 = (f32x4){(float)i1.x, (float)i1.y, (float)i1.z, (float)i1.w} * sv[bj][1]; }
;                     const f32x4 g0 = a0 * rs[ai][m] + bv[bj][0], g1 = a1 * rs[ai][m] + bv[bj][1];
;                     const f16x8 yy = yv[m][bj];
;                     float z[8];
; #pragma unroll
;                     for (int e = 0; e < 4; ++e) { z[e] = (float)yy[e] * __builtin_amdgcn_rcpf(1.f + __builtin_amdgcn_exp2f(-LOG2E * g0[e])); z[4 + e] = (float)yy[4 + e] * __builtin_amdgcn_rcpf(1.f + __builtin_amdgcn_exp2f(-LOG2E * g1[e])); }
;                     if (br == 2) {
; #pragma unroll
;                         for (int e = 0; e < 8; ++e) z[e] += (float)za[bj][e] + (float)zb[bj][e]; }
;                     u32x4 w; w.x = pk2h(z[0], z[1]); w.y = pk2h(z[2], z[3]); w.z = pk2h(z[4], z[5]); w.w = pk2h(z[6], z[7]);
;                     f16* dst = (br == 2) ? merged : Yb;
;                     gst16(dst + off + bj * HALF, w); } } } }
.LBB0_1289:
	v_cvt_f32_i32_e32 v14, v14
	v_cvt_f32_i32_e32 v15, v15
	v_cvt_f32_i32_e32 v18, v10
	v_cvt_f32_i32_e32 v19, v12
	v_mul_f32_e32 v10, v70, v14
	v_mul_f32_e32 v12, v71, v15
	v_fma_f32 v10, v213, v10, v62
	v_cvt_f32_i32_e32 v14, v11
	v_fma_f32 v12, v213, v12, v63
	v_exp_f32_e32 v10, v10
	v_exp_f32_e32 v12, v12
	v_mul_f32_e32 v11, v54, v18
	v_fma_f32 v11, v213, v11, v50
	v_mul_f32_e32 v14, v55, v14
	v_fma_f32 v14, v213, v14, v51
	v_add_f32_e32 v10, 1.0, v10
	v_exp_f32_e32 v15, v11
	v_add_f32_e32 v11, 1.0, v12
	v_cvt_f32_i32_e32 v16, v16
	v_cvt_f32_i32_e32 v17, v17
	v_cvt_f32_i32_e32 v20, v13
	v_rcp_f32_e32 v10, v10
	v_rcp_f32_e32 v11, v11
	s_waitcnt vmcnt(3)
	v_cvt_f32_f16_sdwa v13, v86 dst_sel:DWORD dst_unused:UNUSED_PAD src0_sel:WORD_1
	v_cvt_f32_f16_e32 v12, v86
	v_exp_f32_e32 v18, v14
	v_mul_f32_e32 v17, v73, v17
	v_fmac_f32_e32 v65, v213, v17
	v_pk_mul_f32 v[10:11], v[10:11], v[12:13]
	v_add_f32_e32 v12, 1.0, v18
	v_mul_f32_e32 v13, v72, v16
	v_mul_f32_e32 v18, v56, v19
	v_mul_f32_e32 v19, v57, v20
	v_fma_f32 v13, v213, v13, v64
	v_fma_f32 v18, v213, v18, v52
	v_fmac_f32_e32 v53, v213, v19
	v_mov_b32_e32 v17, v65
	v_mov_b32_e32 v19, v53
	v_exp_f32_e32 v16, v13
	v_exp_f32_e32 v18, v18
	v_exp_f32_e32 v17, v17
	v_exp_f32_e32 v19, v19
	v_add_f32_e32 v14, 1.0, v15
	v_add_f32_e32 v16, 1.0, v16
	v_add_f32_e32 v18, 1.0, v18
	v_add_f32_e32 v17, 1.0, v17
	v_add_f32_e32 v19, 1.0, v19
	v_rcp_f32_e32 v14, v14
	v_rcp_f32_e32 v15, v12
	v_cvt_f32_f16_sdwa v13, v88 dst_sel:DWORD dst_unused:UNUSED_PAD src0_sel:WORD_1
	v_cvt_f32_f16_e32 v12, v88
	v_rcp_f32_e32 v16, v16
	v_rcp_f32_e32 v18, v18
	v_rcp_f32_e32 v17, v17
	v_cvt_f32_f16_sdwa v21, v87 dst_sel:DWORD dst_unused:UNUSED_PAD src0_sel:WORD_1
	v_cvt_f32_f16_e32 v20, v87
	v_rcp_f32_e32 v19, v19
	v_cvt_f32_f16_sdwa v23, v89 dst_sel:DWORD dst_unused:UNUSED_PAD src0_sel:WORD_1
	v_cvt_f32_f16_e32 v22, v89
	v_pk_mul_f32 v[12:13], v[14:15], v[12:13]
	v_pk_mul_f32 v[14:15], v[16:17], v[20:21]
	s_and_b64 vcc, exec, s[36:37]
	v_pk_mul_f32 v[16:17], v[18:19], v[22:23]
	s_cbranch_vccnz .LBB0_1291
	v_cvt_f32_f16_sdwa v19, v58 dst_sel:DWORD dst_unused:UNUSED_PAD src0_sel:WORD_1
	v_cvt_f32_f16_e32 v18, v58
	s_waitcnt vmcnt(1)
	v_cvt_f32_f16_sdwa v21, v66 dst_sel:DWORD dst_unused:UNUSED_PAD src0_sel:WORD_1
	v_cvt_f32_f16_e32 v20, v66
	v_cvt_f32_f16_sdwa v23, v59 dst_sel:DWORD dst_unused:UNUSED_PAD src0_sel:WORD_1
	v_cvt_f32_f16_e32 v22, v59
	v_cvt_f32_f16_sdwa v25, v67 dst_sel:DWORD dst_unused:UNUSED_PAD src0_sel:WORD_1
	v_cvt_f32_f16_e32 v24, v67
	v_cvt_f32_f16_sdwa v51, v60 dst_sel:DWORD dst_unused:UNUSED_PAD src0_sel:WORD_1
	v_cvt_f32_f16_e32 v50, v60
	v_cvt_f32_f16_sdwa v53, v68 dst_sel:DWORD dst_unused:UNUSED_PAD src0_sel:WORD_1
	v_cvt_f32_f16_e32 v52, v68
	v_cvt_f32_f16_sdwa v55, v61 dst_sel:DWORD dst_unused:UNUSED_PAD src0_sel:WORD_1
	v_cvt_f32_f16_e32 v54, v61
	v_cvt_f32_f16_sdwa v57, v69 dst_sel:DWORD dst_unused:UNUSED_PAD src0_sel:WORD_1
	v_cvt_f32_f16_e32 v56, v69
	v_pk_add_f32 v[18:19], v[20:21], v[18:19]
	v_pk_add_f32 v[20:21], v[24:25], v[22:23]
	v_pk_add_f32 v[22:23], v[52:53], v[50:51]
	v_pk_add_f32 v[24:25], v[56:57], v[54:55]
	v_pk_add_f32 v[10:11], v[10:11], v[18:19]
	v_pk_add_f32 v[14:15], v[14:15], v[20:21]
	v_pk_add_f32 v[12:13], v[12:13], v[22:23]
	v_pk_add_f32 v[16:17], v[16:17], v[24:25]
.LBB0_1291:
	v_cvt_f32_i32_e32 v6, v6
	v_cvt_f32_i32_e32 v7, v7
	s_mov_b32 s26, 0x18000
	v_cvt_pk_f16_f32 v10, v10, v11
	v_cvt_pk_f16_f32 v11, v14, v15
	v_add_co_u32_e32 v14, vcc, s26, v106
	v_cvt_pk_f16_f32 v12, v12, v13
	v_cvt_pk_f16_f32 v13, v16, v17
	v_addc_co_u32_e32 v15, vcc, 0, v107, vcc
	s_mov_b64 s[28:29], 0x3800
	v_lshl_add_u64 v[222:223], v[224:225], 0, s[28:29]
	v_cndmask_b32_e64 v222, v14, v222, s[36:37]
	v_cndmask_b32_e64 v223, v15, v223, s[36:37]
	global_store_dwordx4 v[222:223], v[10:13], off
	v_cvt_f32_i32_e32 v8, v8
	v_cvt_f32_i32_e32 v9, v9
	v_cvt_f32_i32_e32 v10, v2
	v_mul_f32_e32 v2, v38, v6
	v_cvt_f32_i32_e32 v11, v4
	v_mul_f32_e32 v4, v39, v7
	v_fma_f32 v2, v213, v2, v34
	v_cvt_f32_i32_e32 v6, v3
	v_fma_f32 v4, v213, v4, v35
	v_exp_f32_e32 v2, v2
	v_exp_f32_e32 v4, v4
	v_mul_f32_e32 v3, v30, v10
	v_fma_f32 v3, v213, v3, v26
	v_mul_f32_e32 v6, v31, v6
	v_fma_f32 v6, v213, v6, v27
	v_add_f32_e32 v2, 1.0, v2
	v_exp_f32_e32 v7, v3
	v_add_f32_e32 v3, 1.0, v4
	v_cvt_f32_i32_e32 v12, v5
	v_rcp_f32_e32 v2, v2
	v_rcp_f32_e32 v3, v3
	s_waitcnt vmcnt(3)
	v_cvt_f32_f16_sdwa v5, v82 dst_sel:DWORD dst_unused:UNUSED_PAD src0_sel:WORD_1
	v_cvt_f32_f16_e32 v4, v82
	v_exp_f32_e32 v10, v6
	v_mul_f32_e32 v9, v41, v9
	v_fmac_f32_e32 v37, v213, v9
	v_pk_mul_f32 v[2:3], v[2:3], v[4:5]
	v_add_f32_e32 v4, 1.0, v10
	v_mul_f32_e32 v5, v40, v8
	v_mul_f32_e32 v10, v32, v11
	v_mul_f32_e32 v11, v33, v12
	v_fma_f32 v5, v213, v5, v36
	v_fma_f32 v10, v213, v10, v28
	v_fmac_f32_e32 v29, v213, v11
	v_mov_b32_e32 v9, v37
	v_mov_b32_e32 v11, v29
	v_exp_f32_e32 v8, v5
	v_exp_f32_e32 v10, v10
	v_exp_f32_e32 v9, v9
	v_exp_f32_e32 v11, v11
	v_add_f32_e32 v6, 1.0, v7
	v_add_f32_e32 v8, 1.0, v8
	v_add_f32_e32 v10, 1.0, v10
	v_add_f32_e32 v9, 1.0, v9
	v_add_f32_e32 v11, 1.0, v11
	v_rcp_f32_e32 v6, v6
	v_rcp_f32_e32 v7, v4
	v_cvt_f32_f16_sdwa v5, v84 dst_sel:DWORD dst_unused:UNUSED_PAD src0_sel:WORD_1
	v_cvt_f32_f16_e32 v4, v84
	v_rcp_f32_e32 v8, v8
	v_rcp_f32_e32 v10, v10
	v_rcp_f32_e32 v9, v9
	v_cvt_f32_f16_sdwa v13, v83 dst_sel:DWORD dst_unused:UNUSED_PAD src0_sel:WORD_1
	v_cvt_f32_f16_e32 v12, v83
	v_rcp_f32_e32 v11, v11
	v_cvt_f32_f16_sdwa v15, v85 dst_sel:DWORD dst_unused:UNUSED_PAD src0_sel:WORD_1
	v_cvt_f32_f16_e32 v14, v85
	v_pk_mul_f32 v[4:5], v[6:7], v[4:5]
	v_pk_mul_f32 v[6:7], v[8:9], v[12:13]
	s_and_b64 vcc, exec, s[36:37]
	v_pk_mul_f32 v[8:9], v[10:11], v[14:15]
	s_cbranch_vccnz .LBB0_1293
	v_cvt_f32_f16_sdwa v11, v42 dst_sel:DWORD dst_unused:UNUSED_PAD src0_sel:WORD_1
	v_cvt_f32_f16_e32 v10, v42
	s_waitcnt vmcnt(1)
	v_cvt_f32_f16_sdwa v13, v46 dst_sel:DWORD dst_unused:UNUSED_PAD src0_sel:WORD_1
	v_cvt_f32_f16_e32 v12, v46
	v_cvt_f32_f16_sdwa v15, v43 dst_sel:DWORD dst_unused:UNUSED_PAD src0_sel:WORD_1
	v_cvt_f32_f16_e32 v14, v43
	v_cvt_f32_f16_sdwa v17, v47 dst_sel:DWORD dst_unused:UNUSED_PAD src0_sel:WORD_1
	v_cvt_f32_f16_e32 v16, v47
	v_cvt_f32_f16_sdwa v19, v44 dst_sel:DWORD dst_unused:UNUSED_PAD src0_sel:WORD_1
	v_cvt_f32_f16_e32 v18, v44
	v_cvt_f32_f16_sdwa v21, v48 dst_sel:DWORD dst_unused:UNUSED_PAD src0_sel:WORD_1
	v_cvt_f32_f16_e32 v20, v48
	v_cvt_f32_f16_sdwa v23, v45 dst_sel:DWORD dst_unused:UNUSED_PAD src0_sel:WORD_1
	v_cvt_f32_f16_e32 v22, v45
	v_cvt_f32_f16_sdwa v25, v49 dst_sel:DWORD dst_unused:UNUSED_PAD src0_sel:WORD_1
	v_cvt_f32_f16_e32 v24, v49
	v_pk_add_f32 v[10:11], v[12:13], v[10:11]
	v_pk_add_f32 v[12:13], v[16:17], v[14:15]
	v_pk_add_f32 v[14:15], v[20:21], v[18:19]
	v_pk_add_f32 v[16:17], v[24:25], v[22:23]
	v_pk_add_f32 v[2:3], v[2:3], v[10:11]
	v_pk_add_f32 v[6:7], v[6:7], v[12:13]
	v_pk_add_f32 v[4:5], v[4:5], v[14:15]
	v_pk_add_f32 v[8:9], v[8:9], v[16:17]
